# stack on the nt cache-policy version: diff epilogue DPP butterflies, SWA sink-load hoist and batched row broadcasts, bf16 pack bit-trick replaced by v_cvt_pk_bf16_f32, SWA ballot recompute trimmed to
# speedup vs baseline: 1.0063x; 1.0063x over previous
; __device__ __forceinline__ unsigned pk2(float lo, float hi) { return f2bf(lo) | (f2bf(hi) << 16); }
; __device__ __forceinline__ float dpp_x1(float v) { return __builtin_bit_cast(float, __builtin_amdgcn_update_dpp(0, __builtin_bit_cast(int, v), 0xB1, 0xF, 0xF, true)); }
; __device__ __forceinline__ float dpp_x2(float v) { return __builtin_bit_cast(float, __builtin_amdgcn_update_dpp(0, __builtin_bit_cast(int, v), 0x4E, 0xF, 0xF, true)); }
; __device__ __forceinline__ float dpp_hm(float v) { return __builtin_bit_cast(float, __builtin_amdgcn_update_dpp(0, __builtin_bit_cast(int, v), 0x141, 0xF, 0xF, true)); }
; __device__ __forceinline__ void qk_vec(bf16_t* p, const u32x4 r, const float (&w)[8], const float (&cs)[8], const float (&sn)[8]) {
;     float x[8] = {bflo(r.x), bfhi(r.x), bflo(r.y), bfhi(r.y), bflo(r.z), bfhi(r.z), bflo(r.w), bfhi(r.w)};
;     float ss = 0.f;
; #pragma unroll
;     for (int e = 0; e < 8; ++e) ss += x[e] * x[e];
;     ss += dpp_x1(ss); ss += dpp_x2(ss); ss += dpp_hm(ss);
;     const float rstd = rsqrtf(ss * (1.f / 64.f) + NORM_EPS);
;     float o[8];
; #pragma unroll
;     for (int e = 0; e < 8; ++e) { const float y = x[e] * rstd * w[e]; o[e] = y * cs[e] + dpp_x2(y) * sn[e]; }
;     u32x4 q; q.x = pk2(o[0], o[1]); q.y = pk2(o[2], o[3]); q.z = pk2(o[4], o[5]); q.w = pk2(o[6], o[7]);
;     *(u32x4*)p = q;
.LBB0_385:
	s_or_b64 exec, exec, s[8:9]
	s_mov_b64 s[8:9], 0x1e00
	v_lshl_add_u64 v[224:225], v[198:199], 0, s[8:9]
	v_lshl_add_u64 v[220:221], v[162:163], 0, s[8:9]
	v_lshl_add_u64 v[216:217], v[134:135], 0, s[8:9]
	v_lshl_add_u64 v[178:179], v[132:133], 0, s[8:9]
	s_mov_b64 s[8:9], 0x1000
	v_lshl_add_u64 v[160:161], v[160:161], 0, s[8:9]
	s_mov_b32 s8, 0x3e38aa3b
	s_waitcnt vmcnt(0)
	v_mov_b32_e32 v16, v107
	v_mov_b32_e32 v20, v103
	v_mov_b32_e32 v21, v105
	v_mov_b32_e32 v107, v108
	v_mov_b32_e32 v12, v111
	v_mov_b32_e32 v13, v113
	v_mov_b32_e32 v111, v112
	v_pk_mul_f32 v[112:113], v[20:21], s[8:9] op_sel_hi:[1,0]
	v_pk_mul_f32 v[20:21], v[106:107], s[8:9] op_sel_hi:[1,0]
	v_lshlrev_b32_e32 v106, 16, v98
	v_and_b32_e32 v108, 0xffff0000, v98
	v_mov_b32_e32 v8, v115
	v_mov_b32_e32 v115, v116
	v_mov_b32_e32 v17, v109
	v_lshlrev_b32_e32 v107, 16, v99
	v_and_b32_e32 v109, 0xffff0000, v99
	v_mov_b32_e32 v98, v106
	v_mov_b32_e32 v99, v108
	v_pk_mul_f32 v[196:197], v[12:13], s[8:9] op_sel_hi:[1,0]
	v_pk_mul_f32 v[12:13], v[114:115], s[8:9] op_sel_hi:[1,0]
	v_pk_mul_f32 v[98:99], v[98:99], v[98:99]
	v_mov_b32_e32 v114, v109
	v_mov_b32_e32 v115, v107
	v_pk_mul_f32 v[114:115], v[114:115], v[114:115]
	v_lshlrev_b32_e32 v116, 16, v100
	v_and_b32_e32 v100, 0xffff0000, v100
	v_add_f32_e32 v67, v98, v99
	v_mov_b32_e32 v242, v100
	v_mov_b32_e32 v243, v116
	v_add_f32_e32 v67, v115, v67
	v_mov_b32_e32 v9, v117
	v_lshlrev_b32_e32 v117, 16, v101
	v_and_b32_e32 v101, 0xffff0000, v101
	v_pk_mul_f32 v[242:243], v[242:243], v[242:243]
	v_add_f32_e32 v67, v114, v67
	v_mov_b32_e32 v244, v101
	v_mov_b32_e32 v245, v117
	v_add_f32_e32 v67, v243, v67
	v_pk_mul_f32 v[244:245], v[244:245], v[244:245]
	v_add_f32_e32 v67, v242, v67
	v_add_f32_e32 v67, v245, v67
	v_add_f32_e32 v67, v244, v67
	v_mov_b32_e32 v103, v104
	v_pk_mul_f32 v[98:99], v[102:103], s[8:9] op_sel_hi:[1,0]
	v_add_f32_dpp v67, v67, v67 quad_perm:[1,0,3,2] row_mask:0xf bank_mask:0xf bound_ctrl:1
	v_pk_mul_f32 v[110:111], v[110:111], s[8:9] op_sel_hi:[1,0]
	s_mov_b64 s[18:19], 0x2200
	v_add_f32_dpp v67, v67, v67 quad_perm:[2,3,0,1] row_mask:0xf bank_mask:0xf bound_ctrl:1
	v_lshl_add_u64 v[222:223], v[198:199], 0, s[18:19]
	v_and_b32_e32 v244, 0xffff0000, v92
	v_add_f32_dpp v67, v67, v67 row_half_mirror row_mask:0xf bank_mask:0xf bound_ctrl:1
	v_fmamk_f32 v67, v67, 0x3c800000, v194
	v_mul_f32_e32 v69, 0x4b800000, v67
	v_cmp_gt_f32_e32 vcc, s66, v67
	v_and_b32_e32 v245, 0xffff0000, v93
	v_mov_b32_e32 v250, v245
	v_cndmask_b32_e32 v67, v67, v69, vcc
	v_rsq_f32_e32 v67, v67
	v_pk_mul_f32 v[8:9], v[8:9], s[8:9] op_sel_hi:[1,0]
	v_pk_mul_f32 v[16:17], v[16:17], s[8:9] op_sel_hi:[1,0]
	s_mov_b32 s8, 0x358637bd
	v_mul_f32_e32 v69, 0x45800000, v67
	v_cndmask_b32_e32 v102, v67, v69, vcc
	v_pk_mul_f32 v[104:105], v[102:103], v[106:107] op_sel_hi:[0,1]
	v_pk_mul_f32 v[104:105], v[98:99], v[104:105]
	v_pk_mul_f32 v[108:109], v[102:103], v[108:109] op_sel_hi:[0,1]
	v_pk_mul_f32 v[108:109], v[112:113], v[108:109]
	v_mov_b32_dpp v106, v104 quad_perm:[2,3,0,1] row_mask:0xf bank_mask:0xf bound_ctrl:1
	v_pk_mul_f32 v[242:243], v[214:215], v[104:105]
	v_mov_b32_dpp v107, v105 quad_perm:[2,3,0,1] row_mask:0xf bank_mask:0xf bound_ctrl:1
	v_mov_b32_dpp v114, v108 quad_perm:[2,3,0,1] row_mask:0xf bank_mask:0xf bound_ctrl:1
	v_pk_fma_f32 v[104:105], v[206:207], v[106:107], v[242:243]
	v_pk_mul_f32 v[106:107], v[212:213], v[108:109]
	v_mov_b32_dpp v115, v109 quad_perm:[2,3,0,1] row_mask:0xf bank_mask:0xf bound_ctrl:1
	v_pk_mul_f32 v[108:109], v[102:103], v[116:117] op_sel_hi:[0,1]
	v_pk_mul_f32 v[108:109], v[110:111], v[108:109]
	v_pk_mul_f32 v[100:101], v[102:103], v[100:101] op_sel_hi:[0,1]
	v_pk_fma_f32 v[106:107], v[202:203], v[114:115], v[106:107]
	v_mov_b32_dpp v114, v108 quad_perm:[2,3,0,1] row_mask:0xf bank_mask:0xf bound_ctrl:1
	v_pk_mul_f32 v[100:101], v[196:197], v[100:101]
	v_pk_mul_f32 v[116:117], v[210:211], v[108:109]
	v_mov_b32_dpp v115, v109 quad_perm:[2,3,0,1] row_mask:0xf bank_mask:0xf bound_ctrl:1
	v_mov_b32_dpp v102, v100 quad_perm:[2,3,0,1] row_mask:0xf bank_mask:0xf bound_ctrl:1
	v_pk_fma_f32 v[108:109], v[200:201], v[114:115], v[116:117]
	v_pk_mul_f32 v[114:115], v[208:209], v[100:101]
	v_mov_b32_dpp v103, v101 quad_perm:[2,3,0,1] row_mask:0xf bank_mask:0xf bound_ctrl:1
	v_pk_fma_f32 v[100:101], v[204:205], v[102:103], v[114:115]
	v_cvt_pk_bf16_f32 v103, v109, v101
	v_cvt_pk_bf16_f32 v102, v108, v100
	v_cvt_pk_bf16_f32 v101, v105, v107
	v_cvt_pk_bf16_f32 v100, v104, v106
	global_store_dwordx4 v[198:199], v[100:103], off offset:3072 nt
	v_lshlrev_b32_e32 v116, 16, v90
	v_and_b32_e32 v198, 0xffff0000, v90
	v_lshlrev_b32_e32 v100, 16, v94
	v_and_b32_e32 v94, 0xffff0000, v94
	v_mov_b32_e32 v102, v100
	v_mov_b32_e32 v103, v94
	v_lshlrev_b32_e32 v117, 16, v91
	v_and_b32_e32 v199, 0xffff0000, v91
	v_mov_b32_e32 v90, v116
	v_mov_b32_e32 v91, v198
	v_pk_mul_f32 v[102:103], v[102:103], v[102:103]
	v_pk_mul_f32 v[90:91], v[90:91], v[90:91]
	v_lshlrev_b32_e32 v101, 16, v95
	v_and_b32_e32 v95, 0xffff0000, v95
	v_mov_b32_e32 v242, v90
	v_mov_b32_e32 v243, v102
	v_mov_b32_e32 v102, v91
	v_mov_b32_e32 v104, v95
	v_mov_b32_e32 v105, v101
	v_pk_add_f32 v[90:91], v[242:243], v[102:103]
	v_mov_b32_e32 v102, v199
	v_mov_b32_e32 v103, v117
	v_pk_mul_f32 v[228:229], v[104:105], v[104:105]
	v_lshlrev_b32_e32 v106, 16, v96
	v_and_b32_e32 v96, 0xffff0000, v96
	v_pk_mul_f32 v[102:103], v[102:103], v[102:103]
	v_lshlrev_b32_e32 v242, 16, v92
	v_mov_b32_e32 v108, v96
	v_mov_b32_e32 v109, v106
	v_lshlrev_b32_e32 v243, 16, v93
	v_mov_b32_e32 v92, v244
	v_mov_b32_e32 v93, v242
	v_mov_b32_e32 v104, v103
	v_mov_b32_e32 v105, v229
; __device__ __forceinline__ unsigned pk2(float lo, float hi) { return f2bf(lo) | (f2bf(hi) << 16); }
; __device__ __forceinline__ float dpp_x1(float v) { return __builtin_bit_cast(float, __builtin_amdgcn_update_dpp(0, __builtin_bit_cast(int, v), 0xB1, 0xF, 0xF, true)); }
; __device__ __forceinline__ float dpp_x2(float v) { return __builtin_bit_cast(float, __builtin_amdgcn_update_dpp(0, __builtin_bit_cast(int, v), 0x4E, 0xF, 0xF, true)); }
; __device__ __forceinline__ float dpp_hm(float v) { return __builtin_bit_cast(float, __builtin_amdgcn_update_dpp(0, __builtin_bit_cast(int, v), 0x141, 0xF, 0xF, true)); }
; __device__ __forceinline__ void qk_vec(bf16_t* p, const u32x4 r, const float (&w)[8], const float (&cs)[8], const float (&sn)[8]) {
;     float x[8] = {bflo(r.x), bfhi(r.x), bflo(r.y), bfhi(r.y), bflo(r.z), bfhi(r.z), bflo(r.w), bfhi(r.w)};
;     float ss = 0.f;
; #pragma unroll
;     for (int e = 0; e < 8; ++e) ss += x[e] * x[e];
;     ss += dpp_x1(ss); ss += dpp_x2(ss); ss += dpp_hm(ss);
;     const float rstd = rsqrtf(ss * (1.f / 64.f) + NORM_EPS);
;     float o[8];
; #pragma unroll
;     for (int e = 0; e < 8; ++e) { const float y = x[e] * rstd * w[e]; o[e] = y * cs[e] + dpp_x2(y) * sn[e]; }
;     u32x4 q; q.x = pk2(o[0], o[1]); q.y = pk2(o[2], o[3]); q.z = pk2(o[4], o[5]); q.w = pk2(o[6], o[7]);
;     *(u32x4*)p = q;
; __device__ __forceinline__ void prep_qk_rows4(KP Pk, Frame& F, int l, int row0) {
;     ...
;     for (int r = 0; r < 4; ++r) { bf16_t* up = U + (size_t)(row0 + r) * NU + 8 * F.lane;
;         qk_vec(up + UC_SQ, raw[r][0], wsq, cs[r], sn[r]); qk_vec(up + UC_DQ, raw[r][1], wdq, cs[r], sn[r]); qk_vec(up + UC_DK, raw[r][2], wdk, cs[r], sn[r]); }
;     qk_vec(U + (size_t)rowk * NU + UC_SK + 8 * (F.lane & 15), rawk, wsk, csk, snk);
	v_lshlrev_b32_e32 v107, 16, v97
	v_and_b32_e32 v97, 0xffff0000, v97
	v_pk_mul_f32 v[108:109], v[108:109], v[108:109]
	v_pk_mul_f32 v[92:93], v[92:93], v[92:93]
	v_pk_add_f32 v[90:91], v[104:105], v[90:91]
	v_mov_b32_e32 v103, v228
	v_mov_b32_e32 v114, v97
	v_mov_b32_e32 v115, v107
	v_mov_b32_e32 v251, v243
	v_pk_add_f32 v[90:91], v[102:103], v[90:91]
	v_mov_b32_e32 v102, v93
	v_mov_b32_e32 v103, v109
	v_pk_mul_f32 v[114:115], v[114:115], v[114:115]
	v_pk_mul_f32 v[250:251], v[250:251], v[250:251]
	v_pk_add_f32 v[90:91], v[102:103], v[90:91]
	v_mov_b32_e32 v93, v108
	v_pk_add_f32 v[90:91], v[92:93], v[90:91]
	v_mov_b32_e32 v92, v251
	v_mov_b32_e32 v93, v115
	v_pk_add_f32 v[90:91], v[92:93], v[90:91]
	v_mov_b32_e32 v251, v114
	v_pk_add_f32 v[90:91], v[250:251], v[90:91]
	v_mov_b32_e32 v189, v85
	v_mov_b32_e32 v191, v81
	v_mov_b32_dpp v93, v91 quad_perm:[1,0,3,2] row_mask:0xf bank_mask:0xf bound_ctrl:1
	v_mov_b32_dpp v92, v90 quad_perm:[1,0,3,2] row_mask:0xf bank_mask:0xf bound_ctrl:1
	v_pk_add_f32 v[90:91], v[90:91], v[92:93]
	v_mov_b32_e32 v177, v73
	v_lshl_add_u64 v[218:219], v[162:163], 0, s[18:19]
	v_mov_b32_dpp v93, v91 quad_perm:[2,3,0,1] row_mask:0xf bank_mask:0xf bound_ctrl:1
	v_mov_b32_dpp v92, v90 quad_perm:[2,3,0,1] row_mask:0xf bank_mask:0xf bound_ctrl:1
	v_pk_add_f32 v[90:91], v[90:91], v[92:93]
	v_lshl_add_u64 v[192:193], v[134:135], 0, s[18:19]
	v_lshl_add_u64 v[164:165], v[132:133], 0, s[18:19]
	v_mov_b32_dpp v93, v91 row_half_mirror row_mask:0xf bank_mask:0xf bound_ctrl:1
	v_mov_b32_dpp v92, v90 row_half_mirror row_mask:0xf bank_mask:0xf bound_ctrl:1
	v_pk_add_f32 v[90:91], v[90:91], v[92:93]
	v_mov_b64_e32 v[92:93], s[8:9]
	s_mov_b32 s8, 0x3c800000
	v_pk_fma_f32 v[102:103], v[90:91], s[8:9], v[92:93] op_sel_hi:[1,0,0]
	v_mov_b32_e32 v90, v34
	v_mul_f32_e32 v67, 0x4b800000, v103
	v_cmp_gt_f32_e32 vcc, s66, v103
	v_mov_b32_e32 v91, v36
	v_mov_b32_e32 v36, v35
	v_cndmask_b32_e32 v67, v103, v67, vcc
	v_rsq_f32_e32 v67, v67
	s_nop 0
	v_mul_f32_e32 v34, 0x45800000, v67
	v_cndmask_b32_e32 v34, v67, v34, vcc
	v_pk_mul_f32 v[100:101], v[34:35], v[100:101] op_sel_hi:[0,1]
	v_pk_mul_f32 v[100:101], v[20:21], v[100:101]
	v_pk_mul_f32 v[94:95], v[34:35], v[94:95] op_sel_hi:[0,1]
	v_pk_mul_f32 v[94:95], v[16:17], v[94:95]
	v_mov_b32_dpp v104, v100 quad_perm:[2,3,0,1] row_mask:0xf bank_mask:0xf bound_ctrl:1
	v_pk_mul_f32 v[114:115], v[214:215], v[100:101]
	v_mov_b32_dpp v105, v101 quad_perm:[2,3,0,1] row_mask:0xf bank_mask:0xf bound_ctrl:1
	v_mov_b32_dpp v108, v94 quad_perm:[2,3,0,1] row_mask:0xf bank_mask:0xf bound_ctrl:1
	v_pk_fma_f32 v[100:101], v[206:207], v[104:105], v[114:115]
	v_pk_mul_f32 v[104:105], v[212:213], v[94:95]
	v_mov_b32_dpp v109, v95 quad_perm:[2,3,0,1] row_mask:0xf bank_mask:0xf bound_ctrl:1
	v_pk_fma_f32 v[94:95], v[202:203], v[108:109], v[104:105]
	v_pk_mul_f32 v[104:105], v[34:35], v[106:107] op_sel_hi:[0,1]
	v_pk_mul_f32 v[104:105], v[12:13], v[104:105]
	v_pk_mul_f32 v[34:35], v[34:35], v[96:97] op_sel_hi:[0,1]
	v_pk_mul_f32 v[34:35], v[8:9], v[34:35]
	v_mov_b32_dpp v106, v104 quad_perm:[2,3,0,1] row_mask:0xf bank_mask:0xf bound_ctrl:1
	v_pk_mul_f32 v[108:109], v[210:211], v[104:105]
	v_mov_b32_dpp v107, v105 quad_perm:[2,3,0,1] row_mask:0xf bank_mask:0xf bound_ctrl:1
	v_mov_b32_dpp v96, v34 quad_perm:[2,3,0,1] row_mask:0xf bank_mask:0xf bound_ctrl:1
	v_pk_fma_f32 v[104:105], v[200:201], v[106:107], v[108:109]
	v_pk_mul_f32 v[106:107], v[208:209], v[34:35]
	v_mov_b32_dpp v97, v35 quad_perm:[2,3,0,1] row_mask:0xf bank_mask:0xf bound_ctrl:1
	v_pk_fma_f32 v[34:35], v[204:205], v[96:97], v[106:107]
	v_cvt_pk_bf16_f32 v96, v104, v34
	v_mul_f32_e32 v34, 0x4b800000, v102
	v_cmp_gt_f32_e32 vcc, s66, v102
	v_bfe_u32 v67, v35, 16, 1
	v_bfe_u32 v79, v94, 16, 1
	v_cndmask_b32_e32 v34, v102, v34, vcc
	v_rsq_f32_e32 v34, v34
	v_add3_u32 v79, v94, v79, s23
	v_add3_u32 v35, v35, v67, s23
	v_cvt_pk_bf16_f32 v67, v100, 0
	v_cvt_pk_bf16_f32 v94, v105, 0
	v_and_or_b32 v97, v35, s95, v94
	v_cvt_pk_bf16_f32 v95, v101, v95
	v_and_or_b32 v94, v79, s95, v67
	v_mul_f32_e32 v35, 0x45800000, v34
	global_store_dwordx4 v[224:225], v[94:97], off nt
	v_and_b32_e32 v108, 0xffff0000, v74
	v_and_b32_e32 v109, 0xffff0000, v75
	v_cndmask_b32_e32 v94, v34, v35, vcc
	v_pk_mul_f32 v[34:35], v[94:95], v[116:117] op_sel_hi:[0,1]
	v_pk_mul_f32 v[100:101], v[94:95], v[198:199] op_sel_hi:[0,1]
	v_pk_mul_f32 v[34:35], v[90:91], v[34:35]
	v_pk_mul_f32 v[100:101], v[36:37], v[100:101]
	v_pk_mul_f32 v[104:105], v[214:215], v[34:35]
	v_mov_b32_dpp v96, v34 quad_perm:[2,3,0,1] row_mask:0xf bank_mask:0xf bound_ctrl:1
	v_mov_b32_dpp v102, v100 quad_perm:[2,3,0,1] row_mask:0xf bank_mask:0xf bound_ctrl:1
	v_mov_b32_dpp v97, v35 quad_perm:[2,3,0,1] row_mask:0xf bank_mask:0xf bound_ctrl:1
	v_pk_mul_f32 v[34:35], v[212:213], v[100:101]
	v_mov_b32_dpp v103, v101 quad_perm:[2,3,0,1] row_mask:0xf bank_mask:0xf bound_ctrl:1
	v_pk_fma_f32 v[100:101], v[202:203], v[102:103], v[34:35]
	v_pk_mul_f32 v[102:103], v[94:95], v[242:243] op_sel_hi:[0,1]
	v_mov_b32_e32 v34, v26
	v_mov_b32_e32 v35, v28
	v_pk_mul_f32 v[94:95], v[94:95], v[244:245] op_sel_hi:[0,1]
	v_mov_b32_e32 v28, v27
	v_pk_mul_f32 v[102:103], v[34:35], v[102:103]
	v_pk_mul_f32 v[94:95], v[28:29], v[94:95]
	v_pk_fma_f32 v[96:97], v[206:207], v[96:97], v[104:105]
	v_mov_b32_dpp v26, v102 quad_perm:[2,3,0,1] row_mask:0xf bank_mask:0xf bound_ctrl:1
	v_mov_b32_dpp v104, v94 quad_perm:[2,3,0,1] row_mask:0xf bank_mask:0xf bound_ctrl:1
	v_pk_mul_f32 v[106:107], v[210:211], v[102:103]
	v_mov_b32_dpp v27, v103 quad_perm:[2,3,0,1] row_mask:0xf bank_mask:0xf bound_ctrl:1
	v_pk_mul_f32 v[102:103], v[208:209], v[94:95]
; __device__ __forceinline__ unsigned pk2(float lo, float hi) { return f2bf(lo) | (f2bf(hi) << 16); }
; __device__ __forceinline__ float dpp_x1(float v) { return __builtin_bit_cast(float, __builtin_amdgcn_update_dpp(0, __builtin_bit_cast(int, v), 0xB1, 0xF, 0xF, true)); }
; __device__ __forceinline__ float dpp_x2(float v) { return __builtin_bit_cast(float, __builtin_amdgcn_update_dpp(0, __builtin_bit_cast(int, v), 0x4E, 0xF, 0xF, true)); }
; __device__ __forceinline__ float dpp_hm(float v) { return __builtin_bit_cast(float, __builtin_amdgcn_update_dpp(0, __builtin_bit_cast(int, v), 0x141, 0xF, 0xF, true)); }
; __device__ __forceinline__ void qk_vec(bf16_t* p, const u32x4 r, const float (&w)[8], const float (&cs)[8], const float (&sn)[8]) {
;     float x[8] = {bflo(r.x), bfhi(r.x), bflo(r.y), bfhi(r.y), bflo(r.z), bfhi(r.z), bflo(r.w), bfhi(r.w)};
;     float ss = 0.f;
; #pragma unroll
;     for (int e = 0; e < 8; ++e) ss += x[e] * x[e];
;     ss += dpp_x1(ss); ss += dpp_x2(ss); ss += dpp_hm(ss);
;     const float rstd = rsqrtf(ss * (1.f / 64.f) + NORM_EPS);
;     float o[8];
; #pragma unroll
;     for (int e = 0; e < 8; ++e) { const float y = x[e] * rstd * w[e]; o[e] = y * cs[e] + dpp_x2(y) * sn[e]; }
;     u32x4 q; q.x = pk2(o[0], o[1]); q.y = pk2(o[2], o[3]); q.z = pk2(o[4], o[5]); q.w = pk2(o[6], o[7]);
;     *(u32x4*)p = q;
; __device__ __forceinline__ void prep_qk_rows4(KP Pk, Frame& F, int l, int row0) {
;     ...
;     for (int r = 0; r < 4; ++r) { bf16_t* up = U + (size_t)(row0 + r) * NU + 8 * F.lane;
;         qk_vec(up + UC_SQ, raw[r][0], wsq, cs[r], sn[r]); qk_vec(up + UC_DQ, raw[r][1], wdq, cs[r], sn[r]); qk_vec(up + UC_DK, raw[r][2], wdk, cs[r], sn[r]); }
;     qk_vec(U + (size_t)rowk * NU + UC_SK + 8 * (F.lane & 15), rawk, wsk, csk, snk);
	v_mov_b32_dpp v105, v95 quad_perm:[2,3,0,1] row_mask:0xf bank_mask:0xf bound_ctrl:1
	v_pk_fma_f32 v[94:95], v[204:205], v[104:105], v[102:103]
	v_pk_fma_f32 v[26:27], v[200:201], v[26:27], v[106:107]
	v_bfe_u32 v67, v95, 16, 1
	v_bfe_u32 v69, v94, 16, 1
	v_bfe_u32 v79, v100, 16, 1
	v_add3_u32 v79, v100, v79, s23
	v_add3_u32 v69, v94, v69, s23
	v_add3_u32 v67, v95, v67, s23
	v_bfe_u32 v71, v101, 16, 1
	v_add3_u32 v71, v101, v71, s23
	v_cvt_pk_bf16_f32 v83, v96, 0
	v_cvt_pk_bf16_f32 v94, v97, 0
	v_cvt_pk_bf16_f32 v26, v26, 0
	v_cvt_pk_bf16_f32 v27, v27, 0
	v_and_or_b32 v97, v67, s95, v27
	v_and_or_b32 v96, v69, s95, v26
	v_and_or_b32 v95, v71, s95, v94
	v_and_or_b32 v94, v79, s95, v83
	v_lshlrev_b32_e32 v26, 16, v86
	v_and_b32_e32 v86, 0xffff0000, v86
	v_lshlrev_b32_e32 v106, 16, v74
	global_store_dwordx4 v[222:223], v[94:97], off nt
	v_lshlrev_b32_e32 v107, 16, v75
	v_mov_b32_e32 v74, v106
	v_mov_b32_e32 v94, v26
	v_mov_b32_e32 v95, v86
	v_mov_b32_e32 v75, v108
	v_pk_mul_f32 v[94:95], v[94:95], v[94:95]
	v_pk_mul_f32 v[74:75], v[74:75], v[74:75]
	v_lshlrev_b32_e32 v27, 16, v87
	v_and_b32_e32 v87, 0xffff0000, v87
	v_mov_b32_e32 v114, v74
	v_mov_b32_e32 v115, v94
	v_mov_b32_e32 v94, v75
	v_mov_b32_e32 v96, v87
	v_mov_b32_e32 v97, v27
	v_pk_add_f32 v[74:75], v[114:115], v[94:95]
	v_mov_b32_e32 v94, v109
	v_mov_b32_e32 v95, v107
	v_pk_mul_f32 v[96:97], v[96:97], v[96:97]
	v_lshlrev_b32_e32 v100, 16, v88
	v_and_b32_e32 v88, 0xffff0000, v88
	v_pk_mul_f32 v[94:95], v[94:95], v[94:95]
	v_lshlrev_b32_e32 v114, 16, v76
	v_and_b32_e32 v116, 0xffff0000, v76
	v_mov_b32_e32 v102, v88
	v_mov_b32_e32 v103, v100
	v_lshlrev_b32_e32 v115, 16, v77
	v_and_b32_e32 v117, 0xffff0000, v77
	v_mov_b32_e32 v76, v116
	v_mov_b32_e32 v77, v114
	v_mov_b32_e32 v200, v95
	v_mov_b32_e32 v201, v97
	v_lshlrev_b32_e32 v101, 16, v89
	v_and_b32_e32 v89, 0xffff0000, v89
	v_pk_mul_f32 v[102:103], v[102:103], v[102:103]
	v_pk_mul_f32 v[76:77], v[76:77], v[76:77]
	v_pk_add_f32 v[74:75], v[200:201], v[74:75]
	v_mov_b32_e32 v95, v96
	v_mov_b32_e32 v104, v89
	v_mov_b32_e32 v105, v101
	v_mov_b32_e32 v198, v117
	v_mov_b32_e32 v199, v115
	v_pk_add_f32 v[74:75], v[94:95], v[74:75]
	v_mov_b32_e32 v94, v77
	v_mov_b32_e32 v95, v103
	v_pk_mul_f32 v[104:105], v[104:105], v[104:105]
	v_pk_mul_f32 v[198:199], v[198:199], v[198:199]
	v_pk_add_f32 v[74:75], v[94:95], v[74:75]
	v_mov_b32_e32 v77, v102
	v_pk_add_f32 v[74:75], v[76:77], v[74:75]
	v_mov_b32_e32 v76, v199
	v_mov_b32_e32 v77, v105
	v_pk_add_f32 v[74:75], v[76:77], v[74:75]
	v_mov_b32_e32 v199, v104
	v_pk_add_f32 v[74:75], v[198:199], v[74:75]
	v_mov_b32_e32 v83, v84
	v_mov_b32_e32 v79, v80
	v_mov_b32_dpp v77, v75 quad_perm:[1,0,3,2] row_mask:0xf bank_mask:0xf bound_ctrl:1
	v_mov_b32_dpp v76, v74 quad_perm:[1,0,3,2] row_mask:0xf bank_mask:0xf bound_ctrl:1
	v_pk_add_f32 v[74:75], v[74:75], v[76:77]
	v_lshlrev_b32_e32 v96, 16, v58
	v_lshlrev_b32_e32 v97, 16, v59
	v_mov_b32_dpp v77, v75 quad_perm:[2,3,0,1] row_mask:0xf bank_mask:0xf bound_ctrl:1
	v_mov_b32_dpp v76, v74 quad_perm:[2,3,0,1] row_mask:0xf bank_mask:0xf bound_ctrl:1
	v_pk_add_f32 v[74:75], v[74:75], v[76:77]
	v_and_b32_e32 v104, 0xffff0000, v60
	v_and_b32_e32 v105, 0xffff0000, v61
	v_mov_b32_dpp v77, v75 row_half_mirror row_mask:0xf bank_mask:0xf bound_ctrl:1
	v_mov_b32_dpp v76, v74 row_half_mirror row_mask:0xf bank_mask:0xf bound_ctrl:1
	v_pk_add_f32 v[74:75], v[74:75], v[76:77]
	s_nop 0
	v_pk_fma_f32 v[74:75], v[74:75], s[8:9], v[92:93] op_sel_hi:[1,0,0]
	s_nop 0
	v_mul_f32_e32 v67, 0x4b800000, v75
	v_cmp_gt_f32_e32 vcc, s66, v75
	s_nop 1
	v_cndmask_b32_e32 v67, v75, v67, vcc
	v_rsq_f32_e32 v67, v67
	s_nop 0
	v_mul_f32_e32 v69, 0x45800000, v67
	v_cndmask_b32_e32 v76, v67, v69, vcc
	v_pk_mul_f32 v[26:27], v[76:77], v[26:27] op_sel_hi:[0,1]
	v_pk_mul_f32 v[26:27], v[98:99], v[26:27]
	v_pk_mul_f32 v[84:85], v[76:77], v[86:87] op_sel_hi:[0,1]
	v_pk_mul_f32 v[84:85], v[112:113], v[84:85]
	v_mov_b32_dpp v80, v26 quad_perm:[2,3,0,1] row_mask:0xf bank_mask:0xf bound_ctrl:1
	v_pk_mul_f32 v[94:95], v[82:83], v[26:27]
	v_mov_b32_dpp v81, v27 quad_perm:[2,3,0,1] row_mask:0xf bank_mask:0xf bound_ctrl:1
	v_mov_b32_dpp v86, v84 quad_perm:[2,3,0,1] row_mask:0xf bank_mask:0xf bound_ctrl:1
	v_pk_fma_f32 v[26:27], v[184:185], v[80:81], v[94:95]
	v_pk_mul_f32 v[80:81], v[188:189], v[84:85]
	v_mov_b32_dpp v87, v85 quad_perm:[2,3,0,1] row_mask:0xf bank_mask:0xf bound_ctrl:1
	v_pk_mul_f32 v[84:85], v[76:77], v[100:101] op_sel_hi:[0,1]
	v_pk_mul_f32 v[84:85], v[110:111], v[84:85]
	v_pk_mul_f32 v[76:77], v[76:77], v[88:89] op_sel_hi:[0,1]
	v_pk_fma_f32 v[80:81], v[182:183], v[86:87], v[80:81]
	v_mov_b32_dpp v86, v84 quad_perm:[2,3,0,1] row_mask:0xf bank_mask:0xf bound_ctrl:1
	v_pk_mul_f32 v[76:77], v[196:197], v[76:77]
	v_pk_mul_f32 v[94:95], v[78:79], v[84:85]
	v_mov_b32_dpp v87, v85 quad_perm:[2,3,0,1] row_mask:0xf bank_mask:0xf bound_ctrl:1
	v_mov_b32_dpp v88, v76 quad_perm:[2,3,0,1] row_mask:0xf bank_mask:0xf bound_ctrl:1
	v_pk_fma_f32 v[84:85], v[180:181], v[86:87], v[94:95]
	v_pk_mul_f32 v[86:87], v[190:191], v[76:77]
	v_mov_b32_dpp v89, v77 quad_perm:[2,3,0,1] row_mask:0xf bank_mask:0xf bound_ctrl:1
	v_pk_fma_f32 v[76:77], v[186:187], v[88:89], v[86:87]
	v_bfe_u32 v71, v81, 16, 1
	v_bfe_u32 v67, v77, 16, 1
	v_bfe_u32 v69, v76, 16, 1
	v_add3_u32 v71, v81, v71, s23
	v_bfe_u32 v75, v80, 16, 1
	v_add3_u32 v69, v76, v69, s23
	v_add3_u32 v67, v77, v67, s23
	v_bfe_u32 v76, v27, 16, 1
	v_add3_u32 v80, v80, v75, s23
	v_bfe_u32 v75, v26, 16, 1
	v_add3_u32 v27, v27, v76, s23
	v_cvt_pk_bf16_f32 v76, v85, 0
	v_add3_u32 v26, v26, v75, s23
	v_cvt_pk_bf16_f32 v75, v84, 0
	v_and_or_b32 v77, v67, s95, v76
; __device__ __forceinline__ unsigned pk2(float lo, float hi) { return f2bf(lo) | (f2bf(hi) << 16); }
; __device__ __forceinline__ float dpp_x1(float v) { return __builtin_bit_cast(float, __builtin_amdgcn_update_dpp(0, __builtin_bit_cast(int, v), 0xB1, 0xF, 0xF, true)); }
; __device__ __forceinline__ float dpp_x2(float v) { return __builtin_bit_cast(float, __builtin_amdgcn_update_dpp(0, __builtin_bit_cast(int, v), 0x4E, 0xF, 0xF, true)); }
; __device__ __forceinline__ float dpp_hm(float v) { return __builtin_bit_cast(float, __builtin_amdgcn_update_dpp(0, __builtin_bit_cast(int, v), 0x141, 0xF, 0xF, true)); }
; __device__ __forceinline__ void qk_vec(bf16_t* p, const u32x4 r, const float (&w)[8], const float (&cs)[8], const float (&sn)[8]) {
;     float x[8] = {bflo(r.x), bfhi(r.x), bflo(r.y), bfhi(r.y), bflo(r.z), bfhi(r.z), bflo(r.w), bfhi(r.w)};
;     float ss = 0.f;
; #pragma unroll
;     for (int e = 0; e < 8; ++e) ss += x[e] * x[e];
;     ss += dpp_x1(ss); ss += dpp_x2(ss); ss += dpp_hm(ss);
;     const float rstd = rsqrtf(ss * (1.f / 64.f) + NORM_EPS);
;     float o[8];
; #pragma unroll
;     for (int e = 0; e < 8; ++e) { const float y = x[e] * rstd * w[e]; o[e] = y * cs[e] + dpp_x2(y) * sn[e]; }
;     u32x4 q; q.x = pk2(o[0], o[1]); q.y = pk2(o[2], o[3]); q.z = pk2(o[4], o[5]); q.w = pk2(o[6], o[7]);
;     *(u32x4*)p = q;
; __device__ __forceinline__ void prep_qk_rows4(KP Pk, Frame& F, int l, int row0) {
;     ...
;     for (int r = 0; r < 4; ++r) { bf16_t* up = U + (size_t)(row0 + r) * NU + 8 * F.lane;
;         qk_vec(up + UC_SQ, raw[r][0], wsq, cs[r], sn[r]); qk_vec(up + UC_DQ, raw[r][1], wdq, cs[r], sn[r]); qk_vec(up + UC_DK, raw[r][2], wdk, cs[r], sn[r]); }
;     qk_vec(U + (size_t)rowk * NU + UC_SK + 8 * (F.lane & 15), rawk, wsk, csk, snk);
	v_mul_f32_e32 v67, 0x4b800000, v74
	v_cmp_gt_f32_e32 vcc, s66, v74
	v_lshrrev_b32_e32 v26, 16, v26
	v_lshrrev_b32_e32 v27, 16, v27
	v_cndmask_b32_e32 v67, v74, v67, vcc
	v_rsq_f32_e32 v67, v67
	v_and_or_b32 v74, v80, s95, v26
	v_and_or_b32 v76, v69, s95, v75
	v_and_or_b32 v75, v71, s95, v27
	v_mul_f32_e32 v26, 0x45800000, v67
	v_cndmask_b32_e32 v26, v67, v26, vcc
	global_store_dwordx4 v[162:163], v[74:77], off offset:3072 nt
	v_pk_mul_f32 v[80:81], v[26:27], v[108:109] op_sel_hi:[0,1]
	v_pk_mul_f32 v[80:81], v[16:17], v[80:81]
	v_pk_mul_f32 v[74:75], v[26:27], v[106:107] op_sel_hi:[0,1]
	v_pk_mul_f32 v[74:75], v[20:21], v[74:75]
	v_mov_b32_dpp v84, v80 quad_perm:[2,3,0,1] row_mask:0xf bank_mask:0xf bound_ctrl:1
	v_pk_mul_f32 v[86:87], v[82:83], v[74:75]
	v_mov_b32_dpp v76, v74 quad_perm:[2,3,0,1] row_mask:0xf bank_mask:0xf bound_ctrl:1
	v_mov_b32_dpp v77, v75 quad_perm:[2,3,0,1] row_mask:0xf bank_mask:0xf bound_ctrl:1
	v_pk_fma_f32 v[74:75], v[184:185], v[76:77], v[86:87]
	v_pk_mul_f32 v[76:77], v[188:189], v[80:81]
	v_mov_b32_dpp v85, v81 quad_perm:[2,3,0,1] row_mask:0xf bank_mask:0xf bound_ctrl:1
	v_pk_mul_f32 v[80:81], v[26:27], v[114:115] op_sel_hi:[0,1]
	v_pk_mul_f32 v[80:81], v[12:13], v[80:81]
	v_pk_mul_f32 v[26:27], v[26:27], v[116:117] op_sel_hi:[0,1]
	v_pk_fma_f32 v[76:77], v[182:183], v[84:85], v[76:77]
	v_mov_b32_dpp v84, v80 quad_perm:[2,3,0,1] row_mask:0xf bank_mask:0xf bound_ctrl:1
	v_pk_mul_f32 v[26:27], v[8:9], v[26:27]
	v_pk_mul_f32 v[88:89], v[78:79], v[80:81]
	v_mov_b32_dpp v85, v81 quad_perm:[2,3,0,1] row_mask:0xf bank_mask:0xf bound_ctrl:1
	v_mov_b32_dpp v86, v26 quad_perm:[2,3,0,1] row_mask:0xf bank_mask:0xf bound_ctrl:1
	v_pk_fma_f32 v[80:81], v[180:181], v[84:85], v[88:89]
	v_pk_mul_f32 v[84:85], v[190:191], v[26:27]
	v_mov_b32_dpp v87, v27 quad_perm:[2,3,0,1] row_mask:0xf bank_mask:0xf bound_ctrl:1
	v_pk_fma_f32 v[26:27], v[186:187], v[86:87], v[84:85]
	v_bfe_u32 v84, v76, 16, 1
	v_bfe_u32 v67, v27, 16, 1
	v_add3_u32 v84, v76, v84, s23
	v_add3_u32 v27, v27, v67, s23
	v_bfe_u32 v71, v77, 16, 1
	v_add3_u32 v71, v77, v71, s23
	v_bfe_u32 v77, v81, 16, 1
	v_cvt_pk_bf16_f32 v76, v80, v26
	v_lshlrev_b32_e32 v26, 16, v62
	v_and_b32_e32 v62, 0xffff0000, v62
	v_and_b32_e32 v100, 0xffff0000, v58
	v_bfe_u32 v69, v75, 16, 1
	v_add3_u32 v77, v81, v77, s23
	v_mov_b32_e32 v80, v26
	v_mov_b32_e32 v81, v62
	v_and_b32_e32 v101, 0xffff0000, v59
	v_mov_b32_e32 v58, v96
	v_mov_b32_e32 v59, v100
	v_add3_u32 v69, v75, v69, s23
	v_lshrrev_b32_e32 v75, 16, v77
	v_pk_mul_f32 v[80:81], v[80:81], v[80:81]
	v_pk_mul_f32 v[58:59], v[58:59], v[58:59]
	v_cvt_pk_bf16_f32 v67, v74, 0
	v_and_or_b32 v77, v27, s95, v75
	v_lshlrev_b32_e32 v27, 16, v63
	v_and_b32_e32 v63, 0xffff0000, v63
	v_mov_b32_e32 v102, v58
	v_mov_b32_e32 v103, v80
	v_mov_b32_e32 v80, v59
	v_and_or_b32 v74, v84, s95, v67
	v_mov_b32_e32 v84, v63
	v_mov_b32_e32 v85, v27
	v_pk_add_f32 v[58:59], v[102:103], v[80:81]
	v_mov_b32_e32 v80, v101
	v_mov_b32_e32 v81, v97
	v_pk_mul_f32 v[84:85], v[84:85], v[84:85]
	v_lshlrev_b32_e32 v86, 16, v64
	v_and_b32_e32 v64, 0xffff0000, v64
	v_pk_mul_f32 v[80:81], v[80:81], v[80:81]
	v_lshlrev_b32_e32 v102, 16, v60
	v_mov_b32_e32 v88, v64
	v_mov_b32_e32 v89, v86
	v_lshlrev_b32_e32 v103, 16, v61
	v_mov_b32_e32 v60, v104
	v_mov_b32_e32 v61, v102
	v_mov_b32_e32 v108, v81
	v_mov_b32_e32 v109, v85
	v_lshlrev_b32_e32 v87, 16, v65
	v_and_b32_e32 v65, 0xffff0000, v65
	v_pk_mul_f32 v[88:89], v[88:89], v[88:89]
	v_pk_mul_f32 v[60:61], v[60:61], v[60:61]
	v_pk_add_f32 v[58:59], v[108:109], v[58:59]
	v_mov_b32_e32 v81, v84
	v_mov_b32_e32 v94, v65
	v_mov_b32_e32 v95, v87
	v_mov_b32_e32 v106, v105
	v_mov_b32_e32 v107, v103
	v_pk_add_f32 v[58:59], v[80:81], v[58:59]
	v_mov_b32_e32 v80, v61
	v_mov_b32_e32 v81, v89
	v_pk_mul_f32 v[94:95], v[94:95], v[94:95]
	v_pk_mul_f32 v[106:107], v[106:107], v[106:107]
	v_pk_add_f32 v[58:59], v[80:81], v[58:59]
	v_mov_b32_e32 v61, v88
	v_pk_add_f32 v[58:59], v[60:61], v[58:59]
	v_mov_b32_e32 v60, v107
	v_mov_b32_e32 v61, v95
	v_pk_add_f32 v[58:59], v[60:61], v[58:59]
	v_mov_b32_e32 v107, v94
	v_pk_add_f32 v[58:59], v[106:107], v[58:59]
	v_lshrrev_b32_e32 v69, 16, v69
	v_and_or_b32 v75, v71, s95, v69
	v_mov_b32_dpp v61, v59 quad_perm:[1,0,3,2] row_mask:0xf bank_mask:0xf bound_ctrl:1
	v_mov_b32_dpp v60, v58 quad_perm:[1,0,3,2] row_mask:0xf bank_mask:0xf bound_ctrl:1
	v_pk_add_f32 v[58:59], v[58:59], v[60:61]
	global_store_dwordx4 v[220:221], v[74:77], off nt
	v_mov_b32_e32 v71, v72
	v_mov_b32_dpp v61, v59 quad_perm:[2,3,0,1] row_mask:0xf bank_mask:0xf bound_ctrl:1
	v_mov_b32_dpp v60, v58 quad_perm:[2,3,0,1] row_mask:0xf bank_mask:0xf bound_ctrl:1
	v_pk_add_f32 v[58:59], v[58:59], v[60:61]
	v_and_b32_e32 v80, 0xffff0000, v52
	v_and_b32_e32 v81, 0xffff0000, v53
	v_mov_b32_dpp v61, v59 row_half_mirror row_mask:0xf bank_mask:0xf bound_ctrl:1
	v_mov_b32_dpp v60, v58 row_half_mirror row_mask:0xf bank_mask:0xf bound_ctrl:1
	v_pk_add_f32 v[58:59], v[58:59], v[60:61]
	s_nop 0
	v_pk_fma_f32 v[58:59], v[58:59], s[8:9], v[92:93] op_sel_hi:[1,0,0]
	s_nop 0
	v_mul_f32_e32 v60, 0x4b800000, v59
	v_cmp_gt_f32_e32 vcc, s66, v59
	s_nop 1
	v_cndmask_b32_e32 v59, v59, v60, vcc
	v_rsq_f32_e32 v59, v59
	s_nop 0
	v_mul_f32_e32 v60, 0x45800000, v59
	v_cndmask_b32_e32 v60, v59, v60, vcc
	v_pk_mul_f32 v[26:27], v[60:61], v[26:27] op_sel_hi:[0,1]
	v_pk_mul_f32 v[26:27], v[90:91], v[26:27]
	v_pk_mul_f32 v[62:63], v[60:61], v[62:63] op_sel_hi:[0,1]
	v_pk_mul_f32 v[62:63], v[36:37], v[62:63]
	v_mov_b32_dpp v72, v26 quad_perm:[2,3,0,1] row_mask:0xf bank_mask:0xf bound_ctrl:1
	v_pk_mul_f32 v[76:77], v[82:83], v[26:27]
	v_mov_b32_dpp v73, v27 quad_perm:[2,3,0,1] row_mask:0xf bank_mask:0xf bound_ctrl:1
; __device__ __forceinline__ unsigned pk2(float lo, float hi) { return f2bf(lo) | (f2bf(hi) << 16); }
; __device__ __forceinline__ float dpp_x1(float v) { return __builtin_bit_cast(float, __builtin_amdgcn_update_dpp(0, __builtin_bit_cast(int, v), 0xB1, 0xF, 0xF, true)); }
; __device__ __forceinline__ float dpp_x2(float v) { return __builtin_bit_cast(float, __builtin_amdgcn_update_dpp(0, __builtin_bit_cast(int, v), 0x4E, 0xF, 0xF, true)); }
; __device__ __forceinline__ float dpp_hm(float v) { return __builtin_bit_cast(float, __builtin_amdgcn_update_dpp(0, __builtin_bit_cast(int, v), 0x141, 0xF, 0xF, true)); }
; __device__ __forceinline__ void qk_vec(bf16_t* p, const u32x4 r, const float (&w)[8], const float (&cs)[8], const float (&sn)[8]) {
;     float x[8] = {bflo(r.x), bfhi(r.x), bflo(r.y), bfhi(r.y), bflo(r.z), bfhi(r.z), bflo(r.w), bfhi(r.w)};
;     float ss = 0.f;
; #pragma unroll
;     for (int e = 0; e < 8; ++e) ss += x[e] * x[e];
;     ss += dpp_x1(ss); ss += dpp_x2(ss); ss += dpp_hm(ss);
;     const float rstd = rsqrtf(ss * (1.f / 64.f) + NORM_EPS);
;     float o[8];
; #pragma unroll
;     for (int e = 0; e < 8; ++e) { const float y = x[e] * rstd * w[e]; o[e] = y * cs[e] + dpp_x2(y) * sn[e]; }
;     u32x4 q; q.x = pk2(o[0], o[1]); q.y = pk2(o[2], o[3]); q.z = pk2(o[4], o[5]); q.w = pk2(o[6], o[7]);
;     *(u32x4*)p = q;
; __device__ __forceinline__ void prep_qk_rows4(KP Pk, Frame& F, int l, int row0) {
;     ...
;     for (int r = 0; r < 4; ++r) { bf16_t* up = U + (size_t)(row0 + r) * NU + 8 * F.lane;
;         qk_vec(up + UC_SQ, raw[r][0], wsq, cs[r], sn[r]); qk_vec(up + UC_DQ, raw[r][1], wdq, cs[r], sn[r]); qk_vec(up + UC_DK, raw[r][2], wdk, cs[r], sn[r]); }
;     qk_vec(U + (size_t)rowk * NU + UC_SK + 8 * (F.lane & 15), rawk, wsk, csk, snk);
	v_mov_b32_dpp v74, v62 quad_perm:[2,3,0,1] row_mask:0xf bank_mask:0xf bound_ctrl:1
	v_pk_fma_f32 v[26:27], v[184:185], v[72:73], v[76:77]
	v_pk_mul_f32 v[72:73], v[188:189], v[62:63]
	v_mov_b32_dpp v75, v63 quad_perm:[2,3,0,1] row_mask:0xf bank_mask:0xf bound_ctrl:1
	v_pk_fma_f32 v[62:63], v[182:183], v[74:75], v[72:73]
	v_pk_mul_f32 v[72:73], v[60:61], v[86:87] op_sel_hi:[0,1]
	v_pk_mul_f32 v[72:73], v[34:35], v[72:73]
	v_pk_mul_f32 v[60:61], v[60:61], v[64:65] op_sel_hi:[0,1]
	v_pk_mul_f32 v[60:61], v[28:29], v[60:61]
	v_mov_b32_dpp v74, v72 quad_perm:[2,3,0,1] row_mask:0xf bank_mask:0xf bound_ctrl:1
	v_pk_mul_f32 v[76:77], v[78:79], v[72:73]
	v_mov_b32_dpp v75, v73 quad_perm:[2,3,0,1] row_mask:0xf bank_mask:0xf bound_ctrl:1
	v_mov_b32_dpp v64, v60 quad_perm:[2,3,0,1] row_mask:0xf bank_mask:0xf bound_ctrl:1
	v_pk_fma_f32 v[72:73], v[180:181], v[74:75], v[76:77]
	v_pk_mul_f32 v[74:75], v[190:191], v[60:61]
	v_mov_b32_dpp v65, v61 quad_perm:[2,3,0,1] row_mask:0xf bank_mask:0xf bound_ctrl:1
	v_pk_fma_f32 v[60:61], v[186:187], v[64:65], v[74:75]
	v_bfe_u32 v67, v62, 16, 1
	v_bfe_u32 v59, v61, 16, 1
	v_add3_u32 v62, v62, v67, s23
	v_bfe_u32 v65, v63, 16, 1
	v_add3_u32 v59, v61, v59, s23
	v_bfe_u32 v61, v26, 16, 1
	v_bfe_u32 v64, v60, 16, 1
	v_add3_u32 v63, v63, v65, s23
	v_bfe_u32 v65, v72, 16, 1
	v_add3_u32 v26, v26, v61, s23
	v_cvt_pk_bf16_f32 v61, v73, 0
	v_add3_u32 v60, v60, v64, s23
	v_bfe_u32 v64, v27, 16, 1
	v_add3_u32 v65, v72, v65, s23
	v_and_or_b32 v61, v59, s95, v61
	v_mul_f32_e32 v59, 0x4b800000, v58
	v_cmp_gt_f32_e32 vcc, s66, v58
	v_add3_u32 v27, v27, v64, s23
	v_lshrrev_b32_e32 v64, 16, v65
	v_cndmask_b32_e32 v58, v58, v59, vcc
	v_and_or_b32 v60, v60, s95, v64
	v_rsq_f32_e32 v64, v58
	v_lshrrev_b32_e32 v26, 16, v26
	v_lshrrev_b32_e32 v27, 16, v27
	v_and_or_b32 v58, v62, s95, v26
	v_mul_f32_e32 v26, 0x45800000, v64
	v_and_or_b32 v59, v63, s95, v27
	v_cndmask_b32_e32 v26, v64, v26, vcc
	global_store_dwordx4 v[218:219], v[58:61], off nt
	v_pk_mul_f32 v[62:63], v[26:27], v[100:101] op_sel_hi:[0,1]
	v_pk_mul_f32 v[62:63], v[112:113], v[62:63]
	v_pk_mul_f32 v[58:59], v[26:27], v[96:97] op_sel_hi:[0,1]
	v_pk_mul_f32 v[58:59], v[98:99], v[58:59]
	v_mov_b32_dpp v64, v62 quad_perm:[2,3,0,1] row_mask:0xf bank_mask:0xf bound_ctrl:1
	v_pk_mul_f32 v[72:73], v[70:71], v[58:59]
	v_mov_b32_dpp v60, v58 quad_perm:[2,3,0,1] row_mask:0xf bank_mask:0xf bound_ctrl:1
	v_mov_b32_dpp v61, v59 quad_perm:[2,3,0,1] row_mask:0xf bank_mask:0xf bound_ctrl:1
	v_pk_fma_f32 v[58:59], v[170:171], v[60:61], v[72:73]
	v_pk_mul_f32 v[60:61], v[176:177], v[62:63]
	v_mov_b32_dpp v65, v63 quad_perm:[2,3,0,1] row_mask:0xf bank_mask:0xf bound_ctrl:1
	v_pk_mul_f32 v[62:63], v[26:27], v[102:103] op_sel_hi:[0,1]
	v_pk_mul_f32 v[62:63], v[110:111], v[62:63]
	v_pk_mul_f32 v[26:27], v[26:27], v[104:105] op_sel_hi:[0,1]
	v_mov_b32_e32 v67, v68
	v_pk_fma_f32 v[60:61], v[168:169], v[64:65], v[60:61]
	v_mov_b32_dpp v64, v62 quad_perm:[2,3,0,1] row_mask:0xf bank_mask:0xf bound_ctrl:1
	v_pk_mul_f32 v[26:27], v[196:197], v[26:27]
	v_pk_mul_f32 v[68:69], v[66:67], v[62:63]
	v_mov_b32_dpp v65, v63 quad_perm:[2,3,0,1] row_mask:0xf bank_mask:0xf bound_ctrl:1
	v_mov_b32_dpp v72, v26 quad_perm:[2,3,0,1] row_mask:0xf bank_mask:0xf bound_ctrl:1
	v_pk_fma_f32 v[62:63], v[166:167], v[64:65], v[68:69]
	v_pk_mul_f32 v[64:65], v[174:175], v[26:27]
	v_mov_b32_dpp v73, v27 quad_perm:[2,3,0,1] row_mask:0xf bank_mask:0xf bound_ctrl:1
	v_pk_fma_f32 v[26:27], v[172:173], v[72:73], v[64:65]
	v_bfe_u32 v69, v60, 16, 1
	v_bfe_u32 v64, v27, 16, 1
	v_add3_u32 v86, v60, v69, s23
	v_add3_u32 v27, v27, v64, s23
	v_bfe_u32 v65, v26, 16, 1
	v_bfe_u32 v68, v61, 16, 1
	v_add3_u32 v26, v26, v65, s23
	v_cvt_pk_bf16_f32 v88, v58, 0
	v_cvt_pk_bf16_f32 v58, v62, 0
	v_add3_u32 v87, v61, v68, s23
	v_bfe_u32 v61, v59, 16, 1
	v_and_or_b32 v58, v26, s95, v58
	v_lshlrev_b32_e32 v26, 16, v54
	v_and_b32_e32 v54, 0xffff0000, v54
	v_lshlrev_b32_e32 v74, 16, v50
	v_and_b32_e32 v76, 0xffff0000, v50
	v_add3_u32 v59, v59, v61, s23
	v_mov_b32_e32 v60, v26
	v_mov_b32_e32 v61, v54
	v_lshlrev_b32_e32 v75, 16, v51
	v_and_b32_e32 v77, 0xffff0000, v51
	v_mov_b32_e32 v50, v74
	v_mov_b32_e32 v51, v76
	v_lshrrev_b32_e32 v89, 16, v59
	v_cvt_pk_bf16_f32 v59, v63, 0
	v_pk_mul_f32 v[60:61], v[60:61], v[60:61]
	v_pk_mul_f32 v[50:51], v[50:51], v[50:51]
	v_and_or_b32 v59, v27, s95, v59
	v_lshlrev_b32_e32 v27, 16, v55
	v_and_b32_e32 v55, 0xffff0000, v55
	v_mov_b32_e32 v78, v50
	v_mov_b32_e32 v79, v60
	v_mov_b32_e32 v60, v51
	v_mov_b32_e32 v62, v55
	v_mov_b32_e32 v63, v27
	v_pk_add_f32 v[50:51], v[78:79], v[60:61]
	v_mov_b32_e32 v60, v77
	v_mov_b32_e32 v61, v75
	v_pk_mul_f32 v[62:63], v[62:63], v[62:63]
	v_lshlrev_b32_e32 v64, 16, v56
	v_and_b32_e32 v68, 0xffff0000, v56
	v_pk_mul_f32 v[60:61], v[60:61], v[60:61]
	v_lshlrev_b32_e32 v78, 16, v52
	v_lshlrev_b32_e32 v65, 16, v57
	v_and_b32_e32 v69, 0xffff0000, v57
	v_mov_b32_e32 v56, v68
	v_mov_b32_e32 v57, v64
	v_lshlrev_b32_e32 v79, 16, v53
	v_mov_b32_e32 v52, v80
	v_mov_b32_e32 v53, v78
	v_mov_b32_e32 v84, v61
	v_mov_b32_e32 v85, v63
	v_pk_mul_f32 v[56:57], v[56:57], v[56:57]
	v_pk_mul_f32 v[52:53], v[52:53], v[52:53]
	v_pk_add_f32 v[50:51], v[84:85], v[50:51]
	v_mov_b32_e32 v61, v62
	v_mov_b32_e32 v72, v69
	v_mov_b32_e32 v73, v65
	v_mov_b32_e32 v82, v81
	v_mov_b32_e32 v83, v79
	v_pk_add_f32 v[50:51], v[60:61], v[50:51]
	v_mov_b32_e32 v60, v53
	v_mov_b32_e32 v61, v57
	v_pk_mul_f32 v[72:73], v[72:73], v[72:73]
	v_pk_mul_f32 v[82:83], v[82:83], v[82:83]
	v_pk_add_f32 v[50:51], v[60:61], v[50:51]
	v_mov_b32_e32 v53, v56
	v_pk_add_f32 v[50:51], v[52:53], v[50:51]
	v_mov_b32_e32 v52, v83
; __device__ __forceinline__ unsigned pk2(float lo, float hi) { return f2bf(lo) | (f2bf(hi) << 16); }
; __device__ __forceinline__ float dpp_x1(float v) { return __builtin_bit_cast(float, __builtin_amdgcn_update_dpp(0, __builtin_bit_cast(int, v), 0xB1, 0xF, 0xF, true)); }
; __device__ __forceinline__ float dpp_x2(float v) { return __builtin_bit_cast(float, __builtin_amdgcn_update_dpp(0, __builtin_bit_cast(int, v), 0x4E, 0xF, 0xF, true)); }
; __device__ __forceinline__ float dpp_hm(float v) { return __builtin_bit_cast(float, __builtin_amdgcn_update_dpp(0, __builtin_bit_cast(int, v), 0x141, 0xF, 0xF, true)); }
; __device__ __forceinline__ void qk_vec(bf16_t* p, const u32x4 r, const float (&w)[8], const float (&cs)[8], const float (&sn)[8]) {
;     float x[8] = {bflo(r.x), bfhi(r.x), bflo(r.y), bfhi(r.y), bflo(r.z), bfhi(r.z), bflo(r.w), bfhi(r.w)};
;     float ss = 0.f;
; #pragma unroll
;     for (int e = 0; e < 8; ++e) ss += x[e] * x[e];
;     ss += dpp_x1(ss); ss += dpp_x2(ss); ss += dpp_hm(ss);
;     const float rstd = rsqrtf(ss * (1.f / 64.f) + NORM_EPS);
;     float o[8];
; #pragma unroll
;     for (int e = 0; e < 8; ++e) { const float y = x[e] * rstd * w[e]; o[e] = y * cs[e] + dpp_x2(y) * sn[e]; }
;     u32x4 q; q.x = pk2(o[0], o[1]); q.y = pk2(o[2], o[3]); q.z = pk2(o[4], o[5]); q.w = pk2(o[6], o[7]);
;     *(u32x4*)p = q;
; __device__ __forceinline__ void prep_qk_rows4(KP Pk, Frame& F, int l, int row0) {
;     ...
;     for (int r = 0; r < 4; ++r) { bf16_t* up = U + (size_t)(row0 + r) * NU + 8 * F.lane;
;         qk_vec(up + UC_SQ, raw[r][0], wsq, cs[r], sn[r]); qk_vec(up + UC_DQ, raw[r][1], wdq, cs[r], sn[r]); qk_vec(up + UC_DK, raw[r][2], wdk, cs[r], sn[r]); }
;     qk_vec(U + (size_t)rowk * NU + UC_SK + 8 * (F.lane & 15), rawk, wsk, csk, snk);
	v_mov_b32_e32 v53, v73
	v_pk_add_f32 v[50:51], v[52:53], v[50:51]
	v_mov_b32_e32 v83, v72
	v_pk_add_f32 v[50:51], v[82:83], v[50:51]
	v_and_or_b32 v57, v87, s95, v89
	v_and_or_b32 v56, v86, s95, v88
	v_mov_b32_dpp v53, v51 quad_perm:[1,0,3,2] row_mask:0xf bank_mask:0xf bound_ctrl:1
	v_mov_b32_dpp v52, v50 quad_perm:[1,0,3,2] row_mask:0xf bank_mask:0xf bound_ctrl:1
	v_pk_add_f32 v[50:51], v[50:51], v[52:53]
	global_store_dwordx4 v[134:135], v[56:59], off offset:3072 nt
	s_nop 0
	v_mov_b32_dpp v53, v51 quad_perm:[2,3,0,1] row_mask:0xf bank_mask:0xf bound_ctrl:1
	v_mov_b32_dpp v52, v50 quad_perm:[2,3,0,1] row_mask:0xf bank_mask:0xf bound_ctrl:1
	v_pk_add_f32 v[50:51], v[50:51], v[52:53]
	s_nop 1
	v_mov_b32_dpp v53, v51 row_half_mirror row_mask:0xf bank_mask:0xf bound_ctrl:1
	v_mov_b32_dpp v52, v50 row_half_mirror row_mask:0xf bank_mask:0xf bound_ctrl:1
	v_pk_add_f32 v[50:51], v[50:51], v[52:53]
	s_nop 0
	v_pk_fma_f32 v[50:51], v[50:51], s[8:9], v[92:93] op_sel_hi:[1,0,0]
	s_nop 0
	v_mul_f32_e32 v52, 0x4b800000, v51
	v_cmp_gt_f32_e32 vcc, s66, v51
	s_nop 1
	v_cndmask_b32_e32 v51, v51, v52, vcc
	v_rsq_f32_e32 v51, v51
	s_nop 0
	v_mul_f32_e32 v52, 0x45800000, v51
	v_cndmask_b32_e32 v52, v51, v52, vcc
	v_pk_mul_f32 v[26:27], v[52:53], v[26:27] op_sel_hi:[0,1]
	v_pk_mul_f32 v[26:27], v[20:21], v[26:27]
	v_pk_mul_f32 v[54:55], v[52:53], v[54:55] op_sel_hi:[0,1]
	v_pk_mul_f32 v[54:55], v[16:17], v[54:55]
	v_mov_b32_dpp v56, v26 quad_perm:[2,3,0,1] row_mask:0xf bank_mask:0xf bound_ctrl:1
	v_pk_mul_f32 v[60:61], v[70:71], v[26:27]
	v_mov_b32_dpp v57, v27 quad_perm:[2,3,0,1] row_mask:0xf bank_mask:0xf bound_ctrl:1
	v_mov_b32_dpp v58, v54 quad_perm:[2,3,0,1] row_mask:0xf bank_mask:0xf bound_ctrl:1
	v_pk_fma_f32 v[26:27], v[170:171], v[56:57], v[60:61]
	v_pk_mul_f32 v[56:57], v[176:177], v[54:55]
	v_mov_b32_dpp v59, v55 quad_perm:[2,3,0,1] row_mask:0xf bank_mask:0xf bound_ctrl:1
	v_pk_fma_f32 v[54:55], v[168:169], v[58:59], v[56:57]
	v_pk_mul_f32 v[56:57], v[52:53], v[64:65] op_sel_hi:[0,1]
	v_pk_mul_f32 v[56:57], v[12:13], v[56:57]
	v_pk_mul_f32 v[52:53], v[52:53], v[68:69] op_sel_hi:[0,1]
	v_pk_mul_f32 v[52:53], v[8:9], v[52:53]
	v_mov_b32_dpp v58, v56 quad_perm:[2,3,0,1] row_mask:0xf bank_mask:0xf bound_ctrl:1
	v_pk_mul_f32 v[62:63], v[66:67], v[56:57]
	v_mov_b32_dpp v59, v57 quad_perm:[2,3,0,1] row_mask:0xf bank_mask:0xf bound_ctrl:1
	v_mov_b32_dpp v60, v52 quad_perm:[2,3,0,1] row_mask:0xf bank_mask:0xf bound_ctrl:1
	v_pk_fma_f32 v[56:57], v[166:167], v[58:59], v[62:63]
	v_pk_mul_f32 v[58:59], v[174:175], v[52:53]
	v_mov_b32_dpp v61, v53 quad_perm:[2,3,0,1] row_mask:0xf bank_mask:0xf bound_ctrl:1
	v_pk_fma_f32 v[52:53], v[172:173], v[60:61], v[58:59]
	v_bfe_u32 v60, v54, 16, 1
	v_bfe_u32 v51, v53, 16, 1
	v_add3_u32 v54, v54, v60, s23
	v_bfe_u32 v60, v57, 16, 1
	v_bfe_u32 v59, v55, 16, 1
	v_add3_u32 v51, v53, v51, s23
	v_bfe_u32 v53, v26, 16, 1
	v_add3_u32 v57, v57, v60, s23
	v_add3_u32 v55, v55, v59, s23
	v_add3_u32 v26, v26, v53, s23
	v_lshrrev_b32_e32 v53, 16, v57
	v_and_or_b32 v53, v51, s95, v53
	v_mul_f32_e32 v51, 0x4b800000, v50
	v_cmp_gt_f32_e32 vcc, s66, v50
	v_cndmask_b32_e32 v50, v50, v51, vcc
	v_cvt_pk_bf16_f32 v52, v56, v52
	v_rsq_f32_e32 v56, v50
	v_lshrrev_b32_e32 v26, 16, v26
	v_cvt_pk_bf16_f32 v27, v27, 0
	v_and_or_b32 v50, v54, s95, v26
	v_mul_f32_e32 v26, 0x45800000, v56
	v_and_or_b32 v51, v55, s95, v27
	v_cndmask_b32_e32 v26, v56, v26, vcc
	global_store_dwordx4 v[216:217], v[50:53], off nt
	v_pk_mul_f32 v[54:55], v[26:27], v[76:77] op_sel_hi:[0,1]
	v_pk_mul_f32 v[54:55], v[36:37], v[54:55]
	v_pk_mul_f32 v[50:51], v[26:27], v[74:75] op_sel_hi:[0,1]
	v_pk_mul_f32 v[50:51], v[90:91], v[50:51]
	v_mov_b32_dpp v56, v54 quad_perm:[2,3,0,1] row_mask:0xf bank_mask:0xf bound_ctrl:1
	v_pk_mul_f32 v[58:59], v[70:71], v[50:51]
	v_mov_b32_dpp v52, v50 quad_perm:[2,3,0,1] row_mask:0xf bank_mask:0xf bound_ctrl:1
	v_mov_b32_dpp v53, v51 quad_perm:[2,3,0,1] row_mask:0xf bank_mask:0xf bound_ctrl:1
	v_pk_fma_f32 v[50:51], v[170:171], v[52:53], v[58:59]
	v_pk_mul_f32 v[52:53], v[176:177], v[54:55]
	v_mov_b32_dpp v57, v55 quad_perm:[2,3,0,1] row_mask:0xf bank_mask:0xf bound_ctrl:1
	v_pk_mul_f32 v[54:55], v[26:27], v[78:79] op_sel_hi:[0,1]
	v_pk_mul_f32 v[54:55], v[34:35], v[54:55]
	v_pk_mul_f32 v[26:27], v[26:27], v[80:81] op_sel_hi:[0,1]
	v_pk_fma_f32 v[52:53], v[168:169], v[56:57], v[52:53]
	v_mov_b32_dpp v56, v54 quad_perm:[2,3,0,1] row_mask:0xf bank_mask:0xf bound_ctrl:1
	v_pk_mul_f32 v[26:27], v[28:29], v[26:27]
	v_pk_mul_f32 v[60:61], v[66:67], v[54:55]
	v_mov_b32_dpp v57, v55 quad_perm:[2,3,0,1] row_mask:0xf bank_mask:0xf bound_ctrl:1
	v_mov_b32_dpp v58, v26 quad_perm:[2,3,0,1] row_mask:0xf bank_mask:0xf bound_ctrl:1
	v_pk_fma_f32 v[54:55], v[166:167], v[56:57], v[60:61]
	v_pk_mul_f32 v[56:57], v[174:175], v[26:27]
	v_mov_b32_dpp v59, v27 quad_perm:[2,3,0,1] row_mask:0xf bank_mask:0xf bound_ctrl:1
	v_pk_fma_f32 v[26:27], v[172:173], v[58:59], v[56:57]
	v_bfe_u32 v59, v52, 16, 1
	v_bfe_u32 v56, v27, 16, 1
	v_add3_u32 v74, v52, v59, s23
	v_add3_u32 v27, v27, v56, s23
	v_bfe_u32 v57, v26, 16, 1
	v_bfe_u32 v58, v53, 16, 1
	v_add3_u32 v26, v26, v57, s23
	v_cvt_pk_bf16_f32 v76, v50, 0
	v_cvt_pk_bf16_f32 v50, v54, 0
	v_add3_u32 v75, v53, v58, s23
	v_bfe_u32 v53, v51, 16, 1
	v_and_or_b32 v50, v26, s95, v50
	v_lshlrev_b32_e32 v26, 16, v46
	v_and_b32_e32 v46, 0xffff0000, v46
	v_lshlrev_b32_e32 v62, 16, v42
	v_and_b32_e32 v64, 0xffff0000, v42
	v_add3_u32 v51, v51, v53, s23
	v_mov_b32_e32 v52, v26
	v_mov_b32_e32 v53, v46
	v_lshlrev_b32_e32 v63, 16, v43
	v_and_b32_e32 v65, 0xffff0000, v43
	v_mov_b32_e32 v42, v62
	v_mov_b32_e32 v43, v64
	v_lshrrev_b32_e32 v77, 16, v51
; __device__ __forceinline__ unsigned pk2(float lo, float hi) { return f2bf(lo) | (f2bf(hi) << 16); }
; __device__ __forceinline__ float dpp_x1(float v) { return __builtin_bit_cast(float, __builtin_amdgcn_update_dpp(0, __builtin_bit_cast(int, v), 0xB1, 0xF, 0xF, true)); }
; __device__ __forceinline__ float dpp_x2(float v) { return __builtin_bit_cast(float, __builtin_amdgcn_update_dpp(0, __builtin_bit_cast(int, v), 0x4E, 0xF, 0xF, true)); }
; __device__ __forceinline__ float dpp_hm(float v) { return __builtin_bit_cast(float, __builtin_amdgcn_update_dpp(0, __builtin_bit_cast(int, v), 0x141, 0xF, 0xF, true)); }
; __device__ __forceinline__ void qk_vec(bf16_t* p, const u32x4 r, const float (&w)[8], const float (&cs)[8], const float (&sn)[8]) {
;     float x[8] = {bflo(r.x), bfhi(r.x), bflo(r.y), bfhi(r.y), bflo(r.z), bfhi(r.z), bflo(r.w), bfhi(r.w)};
;     float ss = 0.f;
; #pragma unroll
;     for (int e = 0; e < 8; ++e) ss += x[e] * x[e];
;     ss += dpp_x1(ss); ss += dpp_x2(ss); ss += dpp_hm(ss);
;     const float rstd = rsqrtf(ss * (1.f / 64.f) + NORM_EPS);
;     float o[8];
; #pragma unroll
;     for (int e = 0; e < 8; ++e) { const float y = x[e] * rstd * w[e]; o[e] = y * cs[e] + dpp_x2(y) * sn[e]; }
;     u32x4 q; q.x = pk2(o[0], o[1]); q.y = pk2(o[2], o[3]); q.z = pk2(o[4], o[5]); q.w = pk2(o[6], o[7]);
;     *(u32x4*)p = q;
; __device__ __forceinline__ void prep_qk_rows4(KP Pk, Frame& F, int l, int row0) {
;     ...
;     for (int r = 0; r < 4; ++r) { bf16_t* up = U + (size_t)(row0 + r) * NU + 8 * F.lane;
;         qk_vec(up + UC_SQ, raw[r][0], wsq, cs[r], sn[r]); qk_vec(up + UC_DQ, raw[r][1], wdq, cs[r], sn[r]); qk_vec(up + UC_DK, raw[r][2], wdk, cs[r], sn[r]); }
;     qk_vec(U + (size_t)rowk * NU + UC_SK + 8 * (F.lane & 15), rawk, wsk, csk, snk);
	v_cvt_pk_bf16_f32 v51, v55, 0
	v_pk_mul_f32 v[52:53], v[52:53], v[52:53]
	v_pk_mul_f32 v[42:43], v[42:43], v[42:43]
	v_and_or_b32 v51, v27, s95, v51
	v_lshlrev_b32_e32 v27, 16, v47
	v_and_b32_e32 v47, 0xffff0000, v47
	v_mov_b32_e32 v66, v42
	v_mov_b32_e32 v67, v52
	v_mov_b32_e32 v52, v43
	v_mov_b32_e32 v54, v47
	v_mov_b32_e32 v55, v27
	v_pk_add_f32 v[42:43], v[66:67], v[52:53]
	v_mov_b32_e32 v52, v65
	v_mov_b32_e32 v53, v63
	v_pk_mul_f32 v[54:55], v[54:55], v[54:55]
	v_lshlrev_b32_e32 v56, 16, v48
	v_and_b32_e32 v58, 0xffff0000, v48
	v_pk_mul_f32 v[52:53], v[52:53], v[52:53]
	v_lshlrev_b32_e32 v66, 16, v44
	v_and_b32_e32 v68, 0xffff0000, v44
	v_lshlrev_b32_e32 v57, 16, v49
	v_and_b32_e32 v59, 0xffff0000, v49
	v_mov_b32_e32 v48, v58
	v_mov_b32_e32 v49, v56
	v_lshlrev_b32_e32 v67, 16, v45
	v_and_b32_e32 v69, 0xffff0000, v45
	v_mov_b32_e32 v44, v68
	v_mov_b32_e32 v45, v66
	v_mov_b32_e32 v72, v53
	v_mov_b32_e32 v73, v55
	v_pk_mul_f32 v[48:49], v[48:49], v[48:49]
	v_pk_mul_f32 v[44:45], v[44:45], v[44:45]
	v_pk_add_f32 v[42:43], v[72:73], v[42:43]
	v_mov_b32_e32 v53, v54
	v_mov_b32_e32 v60, v59
	v_mov_b32_e32 v61, v57
	v_mov_b32_e32 v70, v69
	v_mov_b32_e32 v71, v67
	v_pk_add_f32 v[42:43], v[52:53], v[42:43]
	v_mov_b32_e32 v52, v45
	v_mov_b32_e32 v53, v49
	v_pk_mul_f32 v[60:61], v[60:61], v[60:61]
	v_pk_mul_f32 v[70:71], v[70:71], v[70:71]
	v_pk_add_f32 v[42:43], v[52:53], v[42:43]
	v_mov_b32_e32 v45, v48
	v_pk_add_f32 v[42:43], v[44:45], v[42:43]
	v_mov_b32_e32 v44, v71
	v_mov_b32_e32 v45, v61
	v_pk_add_f32 v[42:43], v[44:45], v[42:43]
	v_mov_b32_e32 v71, v60
	v_pk_add_f32 v[42:43], v[70:71], v[42:43]
	v_and_or_b32 v49, v75, s95, v77
	v_and_or_b32 v48, v74, s95, v76
	v_mov_b32_dpp v45, v43 quad_perm:[1,0,3,2] row_mask:0xf bank_mask:0xf bound_ctrl:1
	v_mov_b32_dpp v44, v42 quad_perm:[1,0,3,2] row_mask:0xf bank_mask:0xf bound_ctrl:1
	v_pk_add_f32 v[42:43], v[42:43], v[44:45]
	global_store_dwordx4 v[192:193], v[48:51], off nt
	s_nop 0
	v_mov_b32_dpp v45, v43 quad_perm:[2,3,0,1] row_mask:0xf bank_mask:0xf bound_ctrl:1
	v_mov_b32_dpp v44, v42 quad_perm:[2,3,0,1] row_mask:0xf bank_mask:0xf bound_ctrl:1
	v_pk_add_f32 v[42:43], v[42:43], v[44:45]
	s_nop 1
	v_mov_b32_dpp v45, v43 row_half_mirror row_mask:0xf bank_mask:0xf bound_ctrl:1
	v_mov_b32_dpp v44, v42 row_half_mirror row_mask:0xf bank_mask:0xf bound_ctrl:1
	v_pk_add_f32 v[42:43], v[42:43], v[44:45]
	s_nop 0
	v_pk_fma_f32 v[42:43], v[42:43], s[8:9], v[92:93] op_sel_hi:[1,0,0]
	s_nop 0
	v_mul_f32_e32 v44, 0x4b800000, v43
	v_cmp_gt_f32_e32 vcc, s66, v43
	s_nop 1
	v_cndmask_b32_e32 v43, v43, v44, vcc
	v_rsq_f32_e32 v43, v43
	s_nop 0
	v_mul_f32_e32 v44, 0x45800000, v43
	v_cndmask_b32_e32 v44, v43, v44, vcc
	v_pk_mul_f32 v[26:27], v[44:45], v[26:27] op_sel_hi:[0,1]
	v_pk_mul_f32 v[26:27], v[98:99], v[26:27]
	v_pk_mul_f32 v[46:47], v[44:45], v[46:47] op_sel_hi:[0,1]
	v_pk_mul_f32 v[46:47], v[112:113], v[46:47]
	v_mov_b32_dpp v48, v26 quad_perm:[2,3,0,1] row_mask:0xf bank_mask:0xf bound_ctrl:1
	v_pk_mul_f32 v[52:53], v[10:11], v[26:27]
	v_mov_b32_dpp v49, v27 quad_perm:[2,3,0,1] row_mask:0xf bank_mask:0xf bound_ctrl:1
	v_mov_b32_dpp v50, v46 quad_perm:[2,3,0,1] row_mask:0xf bank_mask:0xf bound_ctrl:1
	v_pk_fma_f32 v[26:27], v[142:143], v[48:49], v[52:53]
	v_pk_mul_f32 v[48:49], v[150:151], v[46:47]
	v_mov_b32_dpp v51, v47 quad_perm:[2,3,0,1] row_mask:0xf bank_mask:0xf bound_ctrl:1
	v_pk_fma_f32 v[46:47], v[146:147], v[50:51], v[48:49]
	v_pk_mul_f32 v[48:49], v[44:45], v[56:57] op_sel_hi:[0,1]
	v_pk_mul_f32 v[48:49], v[110:111], v[48:49]
	v_pk_mul_f32 v[44:45], v[44:45], v[58:59] op_sel_hi:[0,1]
	v_pk_mul_f32 v[44:45], v[196:197], v[44:45]
	v_mov_b32_dpp v50, v48 quad_perm:[2,3,0,1] row_mask:0xf bank_mask:0xf bound_ctrl:1
	v_pk_mul_f32 v[54:55], v[6:7], v[48:49]
	v_mov_b32_dpp v51, v49 quad_perm:[2,3,0,1] row_mask:0xf bank_mask:0xf bound_ctrl:1
	v_mov_b32_dpp v52, v44 quad_perm:[2,3,0,1] row_mask:0xf bank_mask:0xf bound_ctrl:1
	v_pk_fma_f32 v[48:49], v[140:141], v[50:51], v[54:55]
	v_pk_mul_f32 v[50:51], v[148:149], v[44:45]
	v_mov_b32_dpp v53, v45 quad_perm:[2,3,0,1] row_mask:0xf bank_mask:0xf bound_ctrl:1
	v_pk_fma_f32 v[44:45], v[144:145], v[52:53], v[50:51]
	v_bfe_u32 v52, v46, 16, 1
	v_bfe_u32 v43, v45, 16, 1
	v_add3_u32 v46, v46, v52, s23
	v_bfe_u32 v51, v47, 16, 1
	v_add3_u32 v43, v45, v43, s23
	v_bfe_u32 v45, v26, 16, 1
	v_add3_u32 v47, v47, v51, s23
	v_add3_u32 v26, v26, v45, s23
	v_cvt_pk_bf16_f32 v45, v49, 0
	v_and_or_b32 v45, v43, s95, v45
	v_mul_f32_e32 v43, 0x4b800000, v42
	v_cmp_gt_f32_e32 vcc, s66, v42
	v_cndmask_b32_e32 v42, v42, v43, vcc
	v_cvt_pk_bf16_f32 v44, v48, v44
	v_rsq_f32_e32 v48, v42
	v_lshrrev_b32_e32 v26, 16, v26
	v_cvt_pk_bf16_f32 v27, v27, 0
	v_and_or_b32 v42, v46, s95, v26
	v_mul_f32_e32 v26, 0x45800000, v48
	v_and_or_b32 v43, v47, s95, v27
	v_cndmask_b32_e32 v26, v48, v26, vcc
	global_store_dwordx4 v[132:133], v[42:45], off offset:3072 nt
	s_nop 1
	v_pk_mul_f32 v[42:43], v[26:27], v[62:63] op_sel_hi:[0,1]
	v_pk_mul_f32 v[20:21], v[20:21], v[42:43]
	v_pk_mul_f32 v[44:45], v[26:27], v[64:65] op_sel_hi:[0,1]
	v_pk_mul_f32 v[16:17], v[16:17], v[44:45]
	v_mov_b32_dpp v42, v20 quad_perm:[2,3,0,1] row_mask:0xf bank_mask:0xf bound_ctrl:1
	v_pk_mul_f32 v[46:47], v[10:11], v[20:21]
	v_mov_b32_dpp v43, v21 quad_perm:[2,3,0,1] row_mask:0xf bank_mask:0xf bound_ctrl:1
	v_mov_b32_dpp v44, v16 quad_perm:[2,3,0,1] row_mask:0xf bank_mask:0xf bound_ctrl:1
	v_pk_fma_f32 v[20:21], v[142:143], v[42:43], v[46:47]
	v_pk_mul_f32 v[42:43], v[150:151], v[16:17]
	v_mov_b32_dpp v45, v17 quad_perm:[2,3,0,1] row_mask:0xf bank_mask:0xf bound_ctrl:1
	v_pk_fma_f32 v[16:17], v[146:147], v[44:45], v[42:43]
; __device__ __forceinline__ unsigned pk2(float lo, float hi) { return f2bf(lo) | (f2bf(hi) << 16); }
; __device__ __forceinline__ float dpp_x1(float v) { return __builtin_bit_cast(float, __builtin_amdgcn_update_dpp(0, __builtin_bit_cast(int, v), 0xB1, 0xF, 0xF, true)); }
; __device__ __forceinline__ float dpp_x2(float v) { return __builtin_bit_cast(float, __builtin_amdgcn_update_dpp(0, __builtin_bit_cast(int, v), 0x4E, 0xF, 0xF, true)); }
; __device__ __forceinline__ float dpp_hm(float v) { return __builtin_bit_cast(float, __builtin_amdgcn_update_dpp(0, __builtin_bit_cast(int, v), 0x141, 0xF, 0xF, true)); }
; __device__ __forceinline__ void qk_vec(bf16_t* p, const u32x4 r, const float (&w)[8], const float (&cs)[8], const float (&sn)[8]) {
;     float x[8] = {bflo(r.x), bfhi(r.x), bflo(r.y), bfhi(r.y), bflo(r.z), bfhi(r.z), bflo(r.w), bfhi(r.w)};
;     float ss = 0.f;
; #pragma unroll
;     for (int e = 0; e < 8; ++e) ss += x[e] * x[e];
;     ss += dpp_x1(ss); ss += dpp_x2(ss); ss += dpp_hm(ss);
;     const float rstd = rsqrtf(ss * (1.f / 64.f) + NORM_EPS);
;     float o[8];
; #pragma unroll
;     for (int e = 0; e < 8; ++e) { const float y = x[e] * rstd * w[e]; o[e] = y * cs[e] + dpp_x2(y) * sn[e]; }
;     u32x4 q; q.x = pk2(o[0], o[1]); q.y = pk2(o[2], o[3]); q.z = pk2(o[4], o[5]); q.w = pk2(o[6], o[7]);
;     *(u32x4*)p = q;
; __device__ __forceinline__ void prep_qk_rows4(KP Pk, Frame& F, int l, int row0) {
;     ...
;     for (int r = 0; r < 4; ++r) { bf16_t* up = U + (size_t)(row0 + r) * NU + 8 * F.lane;
;         qk_vec(up + UC_SQ, raw[r][0], wsq, cs[r], sn[r]); qk_vec(up + UC_DQ, raw[r][1], wdq, cs[r], sn[r]); qk_vec(up + UC_DK, raw[r][2], wdk, cs[r], sn[r]); }
;     qk_vec(U + (size_t)rowk * NU + UC_SK + 8 * (F.lane & 15), rawk, wsk, csk, snk);
	v_pk_mul_f32 v[42:43], v[26:27], v[66:67] op_sel_hi:[0,1]
	v_pk_mul_f32 v[12:13], v[12:13], v[42:43]
	v_pk_mul_f32 v[26:27], v[26:27], v[68:69] op_sel_hi:[0,1]
	v_pk_mul_f32 v[8:9], v[8:9], v[26:27]
	v_mov_b32_dpp v42, v12 quad_perm:[2,3,0,1] row_mask:0xf bank_mask:0xf bound_ctrl:1
	v_pk_mul_f32 v[44:45], v[6:7], v[12:13]
	v_mov_b32_dpp v43, v13 quad_perm:[2,3,0,1] row_mask:0xf bank_mask:0xf bound_ctrl:1
	v_mov_b32_dpp v26, v8 quad_perm:[2,3,0,1] row_mask:0xf bank_mask:0xf bound_ctrl:1
	v_pk_fma_f32 v[12:13], v[140:141], v[42:43], v[44:45]
	v_pk_mul_f32 v[42:43], v[148:149], v[8:9]
	v_mov_b32_dpp v27, v9 quad_perm:[2,3,0,1] row_mask:0xf bank_mask:0xf bound_ctrl:1
	v_pk_fma_f32 v[8:9], v[144:145], v[26:27], v[42:43]
	v_bfe_u32 v42, v17, 16, 1
	v_bfe_u32 v26, v9, 16, 1
	v_bfe_u32 v27, v8, 16, 1
	v_bfe_u32 v43, v16, 16, 1
	v_add3_u32 v16, v16, v43, s23
	v_add3_u32 v17, v17, v42, s23
	v_add3_u32 v8, v8, v27, s23
	v_add3_u32 v9, v9, v26, s23
	v_cvt_pk_bf16_f32 v20, v20, 0
	v_cvt_pk_bf16_f32 v21, v21, 0
	v_cvt_pk_bf16_f32 v12, v12, 0
	v_cvt_pk_bf16_f32 v13, v13, 0
	v_and_or_b32 v45, v9, s95, v13
	v_and_or_b32 v44, v8, s95, v12
	v_and_or_b32 v43, v17, s95, v21
	v_and_or_b32 v42, v16, s95, v20
	global_store_dwordx4 v[178:179], v[42:45], off nt
	v_lshlrev_b32_e32 v8, 16, v38
	v_and_b32_e32 v12, 0xffff0000, v38
	v_lshlrev_b32_e32 v44, 16, v30
	v_and_b32_e32 v30, 0xffff0000, v30
	v_mov_b32_e32 v16, v8
	v_mov_b32_e32 v17, v12
	v_mov_b32_e32 v46, v44
	v_mov_b32_e32 v47, v30
	v_lshlrev_b32_e32 v9, 16, v39
	v_and_b32_e32 v13, 0xffff0000, v39
	v_pk_mul_f32 v[16:17], v[16:17], v[16:17]
	v_lshlrev_b32_e32 v45, 16, v31
	v_and_b32_e32 v31, 0xffff0000, v31
	v_pk_mul_f32 v[46:47], v[46:47], v[46:47]
	v_mov_b32_e32 v20, v13
	v_mov_b32_e32 v21, v9
	v_mov_b32_e32 v48, v46
	v_mov_b32_e32 v49, v16
	v_mov_b32_e32 v16, v47
	v_mov_b32_e32 v46, v31
	v_mov_b32_e32 v47, v45
	v_pk_mul_f32 v[20:21], v[20:21], v[20:21]
	v_lshlrev_b32_e32 v26, 16, v40
	v_and_b32_e32 v38, 0xffff0000, v40
	v_pk_add_f32 v[16:17], v[48:49], v[16:17]
	v_pk_mul_f32 v[46:47], v[46:47], v[46:47]
	v_lshlrev_b32_e32 v48, 16, v32
	v_and_b32_e32 v32, 0xffff0000, v32
	v_lshlrev_b32_e32 v27, 16, v41
	v_and_b32_e32 v39, 0xffff0000, v41
	v_mov_b32_e32 v40, v38
	v_mov_b32_e32 v41, v26
	v_mov_b32_e32 v50, v32
	v_mov_b32_e32 v51, v48
	v_mov_b32_e32 v54, v47
	v_mov_b32_e32 v55, v21
	v_pk_mul_f32 v[40:41], v[40:41], v[40:41]
	v_lshlrev_b32_e32 v49, 16, v33
	v_and_b32_e32 v33, 0xffff0000, v33
	v_pk_mul_f32 v[50:51], v[50:51], v[50:51]
	v_pk_add_f32 v[16:17], v[54:55], v[16:17]
	v_mov_b32_e32 v47, v20
	v_mov_b32_e32 v42, v39
	v_mov_b32_e32 v43, v27
	v_mov_b32_e32 v52, v33
	v_mov_b32_e32 v53, v49
	v_pk_add_f32 v[16:17], v[46:47], v[16:17]
	v_mov_b32_e32 v20, v51
	v_mov_b32_e32 v21, v41
	v_pk_mul_f32 v[42:43], v[42:43], v[42:43]
	v_pk_mul_f32 v[52:53], v[52:53], v[52:53]
	v_pk_add_f32 v[16:17], v[20:21], v[16:17]
	v_mov_b32_e32 v51, v40
	v_pk_add_f32 v[16:17], v[50:51], v[16:17]
	v_mov_b32_e32 v20, v53
	v_mov_b32_e32 v21, v43
	v_pk_add_f32 v[16:17], v[20:21], v[16:17]
	v_mov_b32_e32 v53, v42
	v_pk_add_f32 v[16:17], v[52:53], v[16:17]
	s_nop 1
	v_mov_b32_dpp v21, v17 quad_perm:[1,0,3,2] row_mask:0xf bank_mask:0xf bound_ctrl:1
	v_mov_b32_dpp v20, v16 quad_perm:[1,0,3,2] row_mask:0xf bank_mask:0xf bound_ctrl:1
	v_pk_add_f32 v[16:17], v[16:17], v[20:21]
	s_nop 1
	v_mov_b32_dpp v21, v17 quad_perm:[2,3,0,1] row_mask:0xf bank_mask:0xf bound_ctrl:1
	v_mov_b32_dpp v20, v16 quad_perm:[2,3,0,1] row_mask:0xf bank_mask:0xf bound_ctrl:1
	v_pk_add_f32 v[16:17], v[16:17], v[20:21]
	s_nop 1
	v_mov_b32_dpp v21, v17 row_half_mirror row_mask:0xf bank_mask:0xf bound_ctrl:1
	v_mov_b32_dpp v20, v16 row_half_mirror row_mask:0xf bank_mask:0xf bound_ctrl:1
	v_pk_add_f32 v[16:17], v[16:17], v[20:21]
	v_mov_b32_e32 v21, v24
	v_pk_fma_f32 v[16:17], v[16:17], s[8:9], v[92:93] op_sel_hi:[1,0,0]
	v_mov_b32_e32 v24, v23
	v_mul_f32_e32 v20, 0x4b800000, v17
	v_cmp_gt_f32_e32 vcc, s66, v17
	s_mov_b64 s[8:9], 0
	s_nop 0
	v_cndmask_b32_e32 v17, v17, v20, vcc
	v_rsq_f32_e32 v17, v17
	v_mov_b32_e32 v20, v22
	v_mul_f32_e32 v22, 0x45800000, v17
	v_cndmask_b32_e32 v22, v17, v22, vcc
	v_pk_mul_f32 v[8:9], v[22:23], v[8:9] op_sel_hi:[0,1]
	v_pk_mul_f32 v[8:9], v[90:91], v[8:9]
	v_pk_mul_f32 v[12:13], v[22:23], v[12:13] op_sel_hi:[0,1]
; __device__ __forceinline__ unsigned pk2(float lo, float hi) { return f2bf(lo) | (f2bf(hi) << 16); }
; __device__ __forceinline__ float dpp_x1(float v) { return __builtin_bit_cast(float, __builtin_amdgcn_update_dpp(0, __builtin_bit_cast(int, v), 0xB1, 0xF, 0xF, true)); }
; __device__ __forceinline__ float dpp_x2(float v) { return __builtin_bit_cast(float, __builtin_amdgcn_update_dpp(0, __builtin_bit_cast(int, v), 0x4E, 0xF, 0xF, true)); }
; __device__ __forceinline__ float dpp_hm(float v) { return __builtin_bit_cast(float, __builtin_amdgcn_update_dpp(0, __builtin_bit_cast(int, v), 0x141, 0xF, 0xF, true)); }
; __device__ __forceinline__ void qk_vec(bf16_t* p, const u32x4 r, const float (&w)[8], const float (&cs)[8], const float (&sn)[8]) {
;     float x[8] = {bflo(r.x), bfhi(r.x), bflo(r.y), bfhi(r.y), bflo(r.z), bfhi(r.z), bflo(r.w), bfhi(r.w)};
;     float ss = 0.f;
; #pragma unroll
;     for (int e = 0; e < 8; ++e) ss += x[e] * x[e];
;     ss += dpp_x1(ss); ss += dpp_x2(ss); ss += dpp_hm(ss);
;     const float rstd = rsqrtf(ss * (1.f / 64.f) + NORM_EPS);
;     float o[8];
; #pragma unroll
;     for (int e = 0; e < 8; ++e) { const float y = x[e] * rstd * w[e]; o[e] = y * cs[e] + dpp_x2(y) * sn[e]; }
;     u32x4 q; q.x = pk2(o[0], o[1]); q.y = pk2(o[2], o[3]); q.z = pk2(o[4], o[5]); q.w = pk2(o[6], o[7]);
;     *(u32x4*)p = q;
; __device__ __forceinline__ void prep_qk_rows4(KP Pk, Frame& F, int l, int row0) {
;     ...
;     for (int r = 0; r < 4; ++r) { bf16_t* up = U + (size_t)(row0 + r) * NU + 8 * F.lane;
;         qk_vec(up + UC_SQ, raw[r][0], wsq, cs[r], sn[r]); qk_vec(up + UC_DQ, raw[r][1], wdq, cs[r], sn[r]); qk_vec(up + UC_DK, raw[r][2], wdk, cs[r], sn[r]); }
;     qk_vec(U + (size_t)rowk * NU + UC_SK + 8 * (F.lane & 15), rawk, wsk, csk, snk);
	v_pk_mul_f32 v[12:13], v[36:37], v[12:13]
	v_mov_b32_dpp v40, v8 quad_perm:[2,3,0,1] row_mask:0xf bank_mask:0xf bound_ctrl:1
	v_pk_mul_f32 v[10:11], v[10:11], v[8:9]
	v_mov_b32_dpp v41, v9 quad_perm:[2,3,0,1] row_mask:0xf bank_mask:0xf bound_ctrl:1
	v_mov_b32_dpp v36, v12 quad_perm:[2,3,0,1] row_mask:0xf bank_mask:0xf bound_ctrl:1
	v_pk_fma_f32 v[8:9], v[142:143], v[40:41], v[10:11]
	v_pk_mul_f32 v[10:11], v[150:151], v[12:13]
	v_mov_b32_dpp v37, v13 quad_perm:[2,3,0,1] row_mask:0xf bank_mask:0xf bound_ctrl:1
	v_pk_mul_f32 v[12:13], v[22:23], v[26:27] op_sel_hi:[0,1]
	v_pk_mul_f32 v[22:23], v[22:23], v[38:39] op_sel_hi:[0,1]
	v_pk_mul_f32 v[12:13], v[34:35], v[12:13]
	v_pk_mul_f32 v[22:23], v[28:29], v[22:23]
	v_pk_fma_f32 v[10:11], v[146:147], v[36:37], v[10:11]
	v_mov_b32_dpp v26, v12 quad_perm:[2,3,0,1] row_mask:0xf bank_mask:0xf bound_ctrl:1
	v_mov_b32_dpp v28, v22 quad_perm:[2,3,0,1] row_mask:0xf bank_mask:0xf bound_ctrl:1
	v_pk_mul_f32 v[6:7], v[6:7], v[12:13]
	v_mov_b32_dpp v27, v13 quad_perm:[2,3,0,1] row_mask:0xf bank_mask:0xf bound_ctrl:1
	v_pk_mul_f32 v[12:13], v[148:149], v[22:23]
	v_mov_b32_dpp v29, v23 quad_perm:[2,3,0,1] row_mask:0xf bank_mask:0xf bound_ctrl:1
	v_pk_fma_f32 v[6:7], v[140:141], v[26:27], v[6:7]
	v_pk_fma_f32 v[12:13], v[144:145], v[28:29], v[12:13]
	v_bfe_u32 v23, v11, 16, 1
	v_bfe_u32 v17, v13, 16, 1
	v_add3_u32 v11, v11, v23, s23
	v_bfe_u32 v23, v6, 16, 1
	v_bfe_u32 v22, v12, 16, 1
	v_add3_u32 v13, v13, v17, s23
	v_add3_u32 v6, v6, v23, s23
	v_add3_u32 v12, v12, v22, s23
	v_lshrrev_b32_e32 v6, 16, v6
	v_cvt_pk_bf16_f32 v17, v8, 0
	v_and_or_b32 v8, v12, s95, v6
	v_mul_f32_e32 v6, 0x4b800000, v16
	v_cmp_gt_f32_e32 vcc, s66, v16
	v_bfe_u32 v26, v10, 16, 1
	v_add3_u32 v10, v10, v26, s23
	v_cndmask_b32_e32 v6, v16, v6, vcc
	v_bfe_u32 v26, v7, 16, 1
	v_rsq_f32_e32 v12, v6
	v_add3_u32 v7, v7, v26, s23
	v_cvt_pk_bf16_f32 v22, v9, 0
	v_lshrrev_b32_e32 v7, 16, v7
	v_and_or_b32 v9, v13, s95, v7
	v_and_or_b32 v7, v11, s95, v22
	v_and_or_b32 v6, v10, s95, v17
	global_store_dwordx4 v[164:165], v[6:9], off nt
	s_nop 1
	v_mul_f32_e32 v6, 0x45800000, v12
	v_cndmask_b32_e32 v6, v12, v6, vcc
	v_pk_mul_f32 v[8:9], v[6:7], v[44:45] op_sel_hi:[0,1]
	v_pk_mul_f32 v[8:9], v[20:21], v[8:9]
	v_pk_mul_f32 v[12:13], v[6:7], v[30:31] op_sel_hi:[0,1]
	v_pk_mul_f32 v[12:13], v[24:25], v[12:13]
	v_mov_b32_dpp v10, v8 quad_perm:[2,3,0,1] row_mask:0xf bank_mask:0xf bound_ctrl:1
	v_pk_mul_f32 v[18:19], v[18:19], v[8:9]
	v_mov_b32_dpp v11, v9 quad_perm:[2,3,0,1] row_mask:0xf bank_mask:0xf bound_ctrl:1
	v_mov_b32_dpp v16, v12 quad_perm:[2,3,0,1] row_mask:0xf bank_mask:0xf bound_ctrl:1
	v_pk_fma_f32 v[8:9], v[154:155], v[10:11], v[18:19]
	v_pk_mul_f32 v[10:11], v[138:139], v[12:13]
	v_mov_b32_dpp v17, v13 quad_perm:[2,3,0,1] row_mask:0xf bank_mask:0xf bound_ctrl:1
	v_pk_fma_f32 v[10:11], v[156:157], v[16:17], v[10:11]
	v_pk_mul_f32 v[12:13], v[6:7], v[48:49] op_sel_hi:[0,1]
	v_mov_b32_e32 v16, v2
	v_mov_b32_e32 v17, v4
	v_pk_mul_f32 v[6:7], v[6:7], v[32:33] op_sel_hi:[0,1]
	v_mov_b32_e32 v4, v3
	v_pk_mul_f32 v[12:13], v[16:17], v[12:13]
	v_pk_mul_f32 v[4:5], v[4:5], v[6:7]
	v_pk_mul_f32 v[14:15], v[14:15], v[12:13]
	v_mov_b32_dpp v2, v12 quad_perm:[2,3,0,1] row_mask:0xf bank_mask:0xf bound_ctrl:1
	v_mov_b32_dpp v6, v4 quad_perm:[2,3,0,1] row_mask:0xf bank_mask:0xf bound_ctrl:1
	v_mov_b32_dpp v3, v13 quad_perm:[2,3,0,1] row_mask:0xf bank_mask:0xf bound_ctrl:1
	v_pk_mul_f32 v[12:13], v[158:159], v[4:5]
	v_mov_b32_dpp v7, v5 quad_perm:[2,3,0,1] row_mask:0xf bank_mask:0xf bound_ctrl:1
	v_pk_fma_f32 v[4:5], v[136:137], v[6:7], v[12:13]
	v_pk_fma_f32 v[2:3], v[152:153], v[2:3], v[14:15]
	v_bfe_u32 v6, v5, 16, 1
	v_bfe_u32 v7, v4, 16, 1
	v_bfe_u32 v12, v11, 16, 1
	v_bfe_u32 v13, v10, 16, 1
	v_add3_u32 v10, v10, v13, s23
	v_add3_u32 v11, v11, v12, s23
	v_add3_u32 v4, v4, v7, s23
	v_add3_u32 v5, v5, v6, s23
	v_bfe_u32 v12, v2, 16, 1
	v_bfe_u32 v13, v3, 16, 1
	v_add3_u32 v3, v3, v13, s23
	v_add3_u32 v2, v2, v12, s23
	v_cvt_pk_bf16_f32 v6, v8, 0
	v_cvt_pk_bf16_f32 v7, v9, 0
	v_lshrrev_b32_e32 v2, 16, v2
	v_lshrrev_b32_e32 v3, 16, v3
	v_and_or_b32 v5, v5, s95, v3
	v_and_or_b32 v4, v4, s95, v2
	v_and_or_b32 v3, v11, s95, v7
	v_and_or_b32 v2, v10, s95, v6
	global_store_dwordx4 v[160:161], v[2:5], off nt

.LBB0_526:
	v_exp_f32_e32 v99, v99
	v_exp_f32_e32 v83, v83
	s_andn2_b64 s[38:39], exec, s[34:35]
	s_andn2_b64 vcc, exec, s[34:35]
	s_cbranch_vccnz .LBB0_528
	s_movk_i32 s34, 0x7ff
	v_add_u32_e32 v182, 0xbe, v187
	s_movk_i32 s42, 0xfeff
	v_cmp_lt_u32_e32 vcc, s34, v188
	v_cmp_gt_u32_e64 s[40:41], s42, v182
	s_or_b64 s[34:35], vcc, s[40:41]
	v_cndmask_b32_e64 v99, v99, 0, s[34:35]
	v_add_u32_e32 v182, 0xfffff6a1, v186
	s_movk_i32 s34, 0xf800
	v_cmp_gt_u32_e32 vcc, s34, v182
	v_add_u32_e32 v182, 0x9e, v187
	v_cmp_gt_u32_e64 s[40:41], s42, v182
	s_or_b64 s[34:35], vcc, s[40:41]
	v_cndmask_b32_e64 v83, v83, 0, s[34:35]

; #define LAS __attribute__((address_space(3)))
; __device__ __forceinline__ unsigned pk2(float lo, float hi) { return f2bf(lo) | (f2bf(hi) << 16); }
; __device__ __forceinline__ unsigned pk2q(float lo, float hi) { return f2bf(q8(lo)) | (f2bf(q8(hi)) << 16); }
; #define LDS_WAIT() asm volatile("s_waitcnt lgkmcnt(0)" ::: "memory")
; __device__ __forceinline__ void p0_transpose_item(const float* W, int ldw, int srccol0, int k0, bf16_t* dst, int K, LAS float* scr, int lane, bool q = false) {
;     { f32x4 v[8];
; #pragma unroll
;       for (int i = 0; i < 8; ++i) v[i] = *(const f32x4*)(W + (size_t)(k0 + 8 * i + (lane >> 3)) * ldw + srccol0 + 4 * (lane & 7));
; #pragma unroll
;       for (int i = 0; i < 8; ++i) { LAS float* p = scr + (8 * i + (lane >> 3)) * 33 + 4 * (lane & 7); p[0] = v[i][0]; p[1] = v[i][1]; p[2] = v[i][2]; p[3] = v[i][3]; } }
;     LDS_WAIT(); asm volatile("" ::: "memory");
;     const int c = lane & 7;
; #pragma unroll
;     for (int j = 0; j < 4; ++j) { const int n = (lane >> 3) + 8 * j; const LAS float* s = scr + (8 * c) * 33 + n;
;         u32x4 o; if (q) { o.x = pk2q(s[0 * 33], s[1 * 33]); o.y = pk2q(s[2 * 33], s[3 * 33]); o.z = pk2q(s[4 * 33], s[5 * 33]); o.w = pk2q(s[6 * 33], s[7 * 33]); }
;         else { o.x = pk2(s[0 * 33], s[1 * 33]); o.y = pk2(s[2 * 33], s[3 * 33]); o.z = pk2(s[4 * 33], s[5 * 33]); o.w = pk2(s[6 * 33], s[7 * 33]); }
;         *(u32x4*)(dst + (size_t)n * K + k0 + 8 * c) = o; }
;     LDS_WAIT(); asm volatile("" ::: "memory");
; }
.LBB0_847:
	s_andn2_b64 vcc, exec, s[34:35]
	s_cbranch_vccnz .LBB0_849
	s_ashr_i32 s19, s60, 31
	s_mul_i32 s9, s60, 0x2a40000
	s_mul_hi_i32 s5, s60, 0x2a40000
	s_waitcnt lgkmcnt(0)
	s_add_u32 s26, s26, s9
	s_addc_u32 s27, s27, s5
	v_lshlrev_b32_e32 v42, 2, v4
	v_mov_b32_e32 v43, v0
	v_lshl_add_u64 v[42:43], s[26:27], 0, v[42:43]
	s_mov_b64 s[26:27], 0x1800
	v_lshl_add_u64 v[64:65], v[42:43], 0, s[26:27]
	v_lshl_add_u64 v[36:37], v[64:65], 0, v[36:37]
	v_lshl_add_u64 v[34:35], v[64:65], 0, v[34:35]
	global_load_dwordx4 v[42:45], v[36:37], off nt
	v_lshl_add_u64 v[32:33], v[64:65], 0, v[32:33]
	global_load_dwordx4 v[34:37], v[34:35], off nt
	s_mov_b32 s18, s60
	global_load_dwordx4 v[46:49], v[32:33], off nt
	v_mad_i64_i32 v[32:33], s[26:27], v41, s2, v[64:65]
	global_load_dwordx4 v[52:55], v[32:33], off nt
	v_mad_i64_i32 v[32:33], s[26:27], v40, s2, v[64:65]
	global_load_dwordx4 v[56:59], v[32:33], off nt
	v_mad_i64_i32 v[32:33], s[26:27], v39, s2, v[64:65]
	global_load_dwordx4 v[60:63], v[32:33], off nt
	v_mad_i64_i32 v[32:33], s[26:27], v38, s2, v[64:65]
	global_load_dwordx4 v[38:41], v[32:33], off nt
	v_mad_i64_i32 v[32:33], s[26:27], v3, s2, v[64:65]
	global_load_dwordx4 v[64:67], v[32:33], off nt
	v_add_u32_e32 v3, v1, v5
	v_add_u32_e32 v32, 0x420, v3
	s_lshl_b64 s[18:19], s[18:19], 17
	v_readlane_b32 s5, v255, 13
	s_add_u32 s5, s5, s18
	v_readlane_b32 s9, v255, 14
	s_addc_u32 s18, s9, s19
	s_mov_b32 s9, s61
	s_lshl_b64 s[8:9], s[8:9], 1
	s_add_u32 s8, s5, s8
	s_addc_u32 s9, s18, s9
	v_mov_b32_e32 v33, v0
	s_waitcnt vmcnt(7)
	ds_write2_b32 v3, v42, v43 offset1:1
	ds_write2_b32 v3, v44, v45 offset0:2 offset1:3
	s_waitcnt vmcnt(6)
	ds_write2_b32 v32, v34, v35 offset1:1
	v_add_u32_e32 v32, 0x428, v3
	ds_write2_b32 v32, v36, v37 offset1:1
	v_add_u32_e32 v32, 0x840, v3
	s_waitcnt vmcnt(5)
	ds_write2_b32 v32, v46, v47 offset1:1
	v_add_u32_e32 v32, 0x848, v3
	ds_write2_b32 v32, v48, v49 offset1:1
	v_add_u32_e32 v32, 0xc60, v3
	s_waitcnt vmcnt(4)
	ds_write2_b32 v32, v52, v53 offset1:1
	v_add_u32_e32 v32, 0xc68, v3
	ds_write2_b32 v32, v54, v55 offset1:1
	v_add_u32_e32 v32, 0x1080, v3
	s_waitcnt vmcnt(3)
	ds_write2_b32 v32, v56, v57 offset1:1
	v_add_u32_e32 v32, 0x1088, v3
	ds_write2_b32 v32, v58, v59 offset1:1
	v_add_u32_e32 v32, 0x14a0, v3
	s_waitcnt vmcnt(2)
	ds_write2_b32 v32, v60, v61 offset1:1
	v_add_u32_e32 v32, 0x14a8, v3
	ds_write2_b32 v32, v62, v63 offset1:1
	v_add_u32_e32 v32, 0x18c0, v3
	s_waitcnt vmcnt(1)
	ds_write2_b32 v32, v38, v39 offset1:1
	v_add_u32_e32 v32, 0x18c8, v3
	ds_write2_b32 v32, v40, v41 offset1:1
	v_add_u32_e32 v32, 0x1ce0, v3
	v_add_u32_e32 v3, 0x1ce8, v3
	s_waitcnt vmcnt(0)
	ds_write2_b32 v32, v64, v65 offset1:1
	ds_write2_b32 v3, v66, v67 offset1:1
	s_waitcnt lgkmcnt(0)
	ds_read2_b32 v[38:39], v50 offset0:33 offset1:41
	ds_read2_b32 v[40:41], v50 offset1:8
	ds_read2_b32 v[42:43], v50 offset0:66 offset1:74
	ds_read2_b32 v[44:45], v50 offset0:99 offset1:107
	ds_read2_b32 v[46:47], v50 offset0:132 offset1:140
	ds_read2_b32 v[48:49], v50 offset0:165 offset1:173
	ds_read2_b32 v[52:53], v50 offset0:198 offset1:206
	ds_read2_b32 v[54:55], v50 offset0:231 offset1:239
	s_waitcnt lgkmcnt(7)
	s_waitcnt lgkmcnt(6)
	v_cvt_pk_bf16_f32 v34, v40, v38
	s_waitcnt lgkmcnt(5)
	s_waitcnt lgkmcnt(4)
	v_cvt_pk_bf16_f32 v35, v42, v44
	s_waitcnt lgkmcnt(3)
	s_waitcnt lgkmcnt(2)
	v_cvt_pk_bf16_f32 v36, v46, v48
	s_waitcnt lgkmcnt(1)
	v_lshlrev_b32_e32 v32, 1, v6
	s_waitcnt lgkmcnt(0)
	v_lshl_add_u64 v[32:33], s[8:9], 0, v[32:33]
	v_cvt_pk_bf16_f32 v37, v52, v54
	v_lshl_add_u64 v[56:57], v[32:33], 0, v[24:25]
	global_store_dwordx4 v[56:57], v[34:37], off nt
	v_cvt_pk_bf16_f32 v34, v41, v39
	v_cvt_pk_bf16_f32 v35, v43, v45
	v_cvt_pk_bf16_f32 v36, v47, v49
	v_cvt_pk_bf16_f32 v37, v53, v55
	v_lshl_add_u64 v[38:39], v[32:33], 0, v[26:27]
	global_store_dwordx4 v[38:39], v[34:37], off nt
	ds_read2_b32 v[38:39], v50 offset0:49 offset1:57
	ds_read2_b32 v[40:41], v50 offset0:16 offset1:24
	ds_read2_b32 v[42:43], v50 offset0:82 offset1:90
	ds_read2_b32 v[44:45], v50 offset0:115 offset1:123
	ds_read2_b32 v[46:47], v50 offset0:148 offset1:156
	ds_read2_b32 v[48:49], v50 offset0:181 offset1:189
	ds_read2_b32 v[52:53], v50 offset0:214 offset1:222
	ds_read2_b32 v[54:55], v50 offset0:247 offset1:255
	s_waitcnt lgkmcnt(7)
	s_waitcnt lgkmcnt(6)
	v_cvt_pk_bf16_f32 v34, v40, v38
	s_waitcnt lgkmcnt(5)
	s_waitcnt lgkmcnt(4)
	v_cvt_pk_bf16_f32 v35, v42, v44
	s_waitcnt lgkmcnt(3)
	s_waitcnt lgkmcnt(2)
	v_cvt_pk_bf16_f32 v36, v46, v48
	s_waitcnt lgkmcnt(1)
	s_waitcnt lgkmcnt(0)
	v_cvt_pk_bf16_f32 v37, v52, v54
	v_lshl_add_u64 v[56:57], v[32:33], 0, v[28:29]
	global_store_dwordx4 v[56:57], v[34:37], off nt
	v_cvt_pk_bf16_f32 v34, v41, v39
	v_cvt_pk_bf16_f32 v35, v43, v45
	v_cvt_pk_bf16_f32 v36, v47, v49
	v_bfe_u32 v37, v55, 16, 1
	v_cvt_pk_bf16_f32 v3, v53, 0
	v_add3_u32 v37, v55, v37, s23
	v_and_or_b32 v37, v37, s95, v3
	v_lshl_add_u64 v[32:33], v[32:33], 0, v[30:31]
	global_store_dwordx4 v[32:33], v[34:37], off nt
	s_waitcnt lgkmcnt(0)

; #define LAS __attribute__((address_space(3)))
; __device__ __forceinline__ unsigned pk2(float lo, float hi) { return f2bf(lo) | (f2bf(hi) << 16); }
; __device__ __forceinline__ unsigned pk2q(float lo, float hi) { return f2bf(q8(lo)) | (f2bf(q8(hi)) << 16); }
; #define LDS_WAIT() asm volatile("s_waitcnt lgkmcnt(0)" ::: "memory")
; __device__ __forceinline__ void p0_transpose_item(const float* W, int ldw, int srccol0, int k0, bf16_t* dst, int K, LAS float* scr, int lane, bool q = false) {
;     { f32x4 v[8];
; #pragma unroll
;       for (int i = 0; i < 8; ++i) v[i] = *(const f32x4*)(W + (size_t)(k0 + 8 * i + (lane >> 3)) * ldw + srccol0 + 4 * (lane & 7));
; #pragma unroll
;       for (int i = 0; i < 8; ++i) { LAS float* p = scr + (8 * i + (lane >> 3)) * 33 + 4 * (lane & 7); p[0] = v[i][0]; p[1] = v[i][1]; p[2] = v[i][2]; p[3] = v[i][3]; } }
;     LDS_WAIT(); asm volatile("" ::: "memory");
;     const int c = lane & 7;
; #pragma unroll
;     for (int j = 0; j < 4; ++j) { const int n = (lane >> 3) + 8 * j; const LAS float* s = scr + (8 * c) * 33 + n;
;         u32x4 o; if (q) { o.x = pk2q(s[0 * 33], s[1 * 33]); o.y = pk2q(s[2 * 33], s[3 * 33]); o.z = pk2q(s[4 * 33], s[5 * 33]); o.w = pk2q(s[6 * 33], s[7 * 33]); }
;         else { o.x = pk2(s[0 * 33], s[1 * 33]); o.y = pk2(s[2 * 33], s[3 * 33]); o.z = pk2(s[4 * 33], s[5 * 33]); o.w = pk2(s[6 * 33], s[7 * 33]); }
;         *(u32x4*)(dst + (size_t)n * K + k0 + 8 * c) = o; }
;     LDS_WAIT(); asm volatile("" ::: "memory");
; }
.LBB0_853:
	s_andn2_b64 vcc, exec, s[40:41]
	s_cbranch_vccnz .LBB0_819
	s_mul_hi_i32 s5, s60, 0x2a40000
	s_waitcnt lgkmcnt(0)
	s_add_u32 s9, s38, s4
	s_addc_u32 s18, s39, s5
	s_mul_i32 s4, s60, 0x1500
	s_ashr_i32 s19, s34, 31
	s_mul_hi_i32 s5, s60, 0x1500
	s_add_u32 s4, s4, s34
	s_addc_u32 s5, s5, s19
	s_lshl_b64 s[4:5], s[4:5], 12
	v_readlane_b32 s19, v255, 15
	s_add_u32 s19, s19, s4
	v_readlane_b32 s4, v255, 16
	s_addc_u32 s34, s4, s5
	s_lshl_b64 s[4:5], s[26:27], 2
	s_add_u32 s4, s9, s4
	s_addc_u32 s5, s18, s5
	v_mov_b32_e32 v37, v0
	v_lshl_add_u64 v[78:79], s[4:5], 0, v[36:37]
	v_lshl_add_u64 v[34:35], v[78:79], 0, v[34:35]
	global_load_dwordx4 v[34:37], v[34:35], off nt
	v_lshl_add_u64 v[32:33], v[78:79], 0, v[32:33]
	global_load_dwordx4 v[38:41], v[32:33], off nt
	v_mad_i64_i32 v[32:33], s[4:5], v62, s2, v[78:79]
	global_load_dwordx4 v[62:65], v[32:33], off nt
	v_mad_i64_i32 v[32:33], s[4:5], v61, s2, v[78:79]
	global_load_dwordx4 v[66:69], v[32:33], off nt
	v_mad_i64_i32 v[32:33], s[4:5], v60, s2, v[78:79]
	global_load_dwordx4 v[70:73], v[32:33], off nt
	v_mad_i64_i32 v[32:33], s[4:5], v59, s2, v[78:79]
	global_load_dwordx4 v[74:77], v[32:33], off nt
	v_mad_i64_i32 v[32:33], s[4:5], v58, s2, v[78:79]
	global_load_dwordx4 v[58:61], v[32:33], off nt
	v_mad_i64_i32 v[32:33], s[4:5], v57, s2, v[78:79]
	global_load_dwordx4 v[78:81], v[32:33], off nt
	s_ashr_i32 s9, s8, 31
	s_lshl_b64 s[4:5], s[8:9], 1
	s_add_u32 s8, s19, s4
	s_addc_u32 s9, s34, s5
	v_lshlrev_b32_e32 v32, 1, v6
	v_mov_b32_e32 v33, v0
	v_lshl_add_u64 v[32:33], s[8:9], 0, v[32:33]
	s_waitcnt vmcnt(7)
	ds_write2_b32 v3, v34, v35 offset1:1
	ds_write2_b32 v3, v36, v37 offset0:2 offset1:3
	s_waitcnt vmcnt(6)
	ds_write2_b32 v42, v38, v39 offset1:1
	ds_write2_b32 v43, v40, v41 offset1:1
	s_waitcnt vmcnt(5)
	ds_write2_b32 v44, v62, v63 offset1:1
	ds_write2_b32 v45, v64, v65 offset1:1
	s_waitcnt vmcnt(4)
	ds_write2_b32 v46, v66, v67 offset1:1
	ds_write2_b32 v47, v68, v69 offset1:1
	s_waitcnt vmcnt(3)
	ds_write2_b32 v48, v70, v71 offset1:1
	ds_write2_b32 v49, v72, v73 offset1:1
	s_waitcnt vmcnt(2)
	ds_write2_b32 v51, v74, v75 offset1:1
	ds_write2_b32 v52, v76, v77 offset1:1
	s_waitcnt vmcnt(1)
	ds_write2_b32 v53, v58, v59 offset1:1
	ds_write2_b32 v54, v60, v61 offset1:1
	s_waitcnt vmcnt(0)
	ds_write2_b32 v55, v78, v79 offset1:1
	ds_write2_b32 v56, v80, v81 offset1:1
	s_waitcnt lgkmcnt(0)
	ds_read2_b32 v[46:47], v50 offset0:33 offset1:41
	ds_read2_b32 v[48:49], v50 offset1:8
	v_lshl_add_u64 v[56:57], v[32:33], 0, v[24:25]
	s_waitcnt lgkmcnt(1)
	s_waitcnt lgkmcnt(0)
	v_cvt_pk_bf16_f32 v52, v48, v46
	ds_read2_b32 v[36:37], v50 offset0:66 offset1:74
	ds_read2_b32 v[34:35], v50 offset0:99 offset1:107
	ds_read2_b32 v[40:41], v50 offset0:132 offset1:140
	ds_read2_b32 v[38:39], v50 offset0:165 offset1:173
	ds_read2_b32 v[44:45], v50 offset0:198 offset1:206
	ds_read2_b32 v[42:43], v50 offset0:231 offset1:239
	s_waitcnt lgkmcnt(5)
	s_waitcnt lgkmcnt(4)
	v_cvt_pk_bf16_f32 v53, v36, v34
	s_waitcnt lgkmcnt(3)
	s_waitcnt lgkmcnt(2)
	v_cvt_pk_bf16_f32 v54, v40, v38
	s_waitcnt lgkmcnt(1)
	s_waitcnt lgkmcnt(0)
	v_cvt_pk_bf16_f32 v55, v44, v42
	v_cvt_pk_bf16_f32 v34, v49, v47
	v_cvt_pk_bf16_f32 v35, v37, v35
	v_cvt_pk_bf16_f32 v36, v41, v39
	v_cvt_pk_bf16_f32 v37, v45, v43
	v_lshl_add_u64 v[38:39], v[32:33], 0, v[26:27]
	global_store_dwordx4 v[56:57], v[52:55], off nt
	global_store_dwordx4 v[38:39], v[34:37], off nt
	ds_read2_b32 v[38:39], v50 offset0:49 offset1:57
	ds_read2_b32 v[40:41], v50 offset0:16 offset1:24
	ds_read2_b32 v[42:43], v50 offset0:82 offset1:90
	ds_read2_b32 v[44:45], v50 offset0:115 offset1:123
	ds_read2_b32 v[46:47], v50 offset0:148 offset1:156
	ds_read2_b32 v[48:49], v50 offset0:181 offset1:189
	ds_read2_b32 v[52:53], v50 offset0:214 offset1:222
	ds_read2_b32 v[54:55], v50 offset0:247 offset1:255
	s_waitcnt lgkmcnt(7)
	s_waitcnt lgkmcnt(6)
	v_cvt_pk_bf16_f32 v34, v40, v38
	s_waitcnt lgkmcnt(5)
	s_waitcnt lgkmcnt(4)
	v_cvt_pk_bf16_f32 v35, v42, v44
	s_waitcnt lgkmcnt(3)
	s_waitcnt lgkmcnt(2)
	v_cvt_pk_bf16_f32 v36, v46, v48
	s_waitcnt lgkmcnt(1)
	s_waitcnt lgkmcnt(0)
	v_cvt_pk_bf16_f32 v37, v52, v54
	v_lshl_add_u64 v[56:57], v[32:33], 0, v[28:29]
	global_store_dwordx4 v[56:57], v[34:37], off nt
	v_cvt_pk_bf16_f32 v34, v41, v39
	v_cvt_pk_bf16_f32 v35, v43, v45
	v_cvt_pk_bf16_f32 v36, v47, v49
	v_bfe_u32 v37, v55, 16, 1
	v_cvt_pk_bf16_f32 v3, v53, 0
	v_add3_u32 v37, v55, v37, s23
	v_and_or_b32 v37, v37, s95, v3
	v_lshl_add_u64 v[32:33], v[32:33], 0, v[30:31]
	global_store_dwordx4 v[32:33], v[34:37], off nt
	s_waitcnt lgkmcnt(0)
	s_branch .LBB0_819
